# speedup vs baseline: 1.0026x; 1.0026x over previous
.Lg_nostag:
	v_add_u32_e32 v6, s33, v5
	ds_read_b128 v[72:75], v6 offset:0
	ds_read_b128 v[76:79], v6 offset:2048
	ds_read_b128 v[80:83], v6 offset:4096
	ds_read_b128 v[84:87], v6 offset:6144
	ds_read_b128 v[88:91], v4 offset:0
	ds_read_b128 v[92:95], v4 offset:2048
	ds_read_b128 v[96:99], v4 offset:4096
	ds_read_b128 v[100:103], v4 offset:6144
	ds_read_b128 v[104:107], v4 offset:8192
	ds_read_b128 v[108:111], v4 offset:10240
	ds_read_b128 v[112:115], v4 offset:12288
	ds_read_b128 v[116:119], v4 offset:14336
	s_waitcnt vmcnt(18)
	v_cvt_pk_bf16_f32 v40, v40, v41
	v_cvt_pk_bf16_f32 v41, v42, v43
	v_cvt_pk_bf16_f32 v44, v44, v45
	v_cvt_pk_bf16_f32 v45, v46, v47
	ds_write2st64_b64 v3, v[40:41], v[44:45] offset0:64 offset1:72
	s_waitcnt vmcnt(16)
	v_cvt_pk_bf16_f32 v48, v48, v49
	v_cvt_pk_bf16_f32 v49, v50, v51
	v_cvt_pk_bf16_f32 v52, v52, v53
	v_cvt_pk_bf16_f32 v53, v54, v55
	ds_write2st64_b64 v3, v[48:49], v[52:53] offset0:80 offset1:88
	s_waitcnt lgkmcnt(0)
	s_barrier
	v_mfma_f32_16x16x32_bf16 v[120:123], v[72:75], v[88:91], v[120:123]
	s_min_u32 s40, s25, 31
	s_bitcmp1_b32 s40, 4
	s_cselect_b32 s41, s23, s22
	s_lshl_b32 s42, s40, 23
	s_and_b32 s42, s42, 0x7000000
	s_or_b32 s41, s41, s42
	s_lshl_b32 s42, s40, 8
	s_and_b32 s42, s42, 0x100
	s_or_b32 s41, s41, s42
	s_sub_u32 s43, s25, 1
	s_min_u32 s43, s43, 31
	s_and_b32 s43, s43, 15
	s_lshl_b32 s43, s43, 15
	s_add_u32 s44, s43, s24
	v_mfma_f32_16x16x32_bf16 v[124:127], v[76:79], v[88:91], v[124:127]
	v_mfma_f32_16x16x32_bf16 v[128:131], v[80:83], v[88:91], v[128:131]
	v_mfma_f32_16x16x32_bf16 v[132:135], v[84:87], v[88:91], v[132:135]
	buffer_load_dwordx4 v[40:43], v1, s[4:7], s41 offen sc0 nt
	v_mfma_f32_16x16x32_bf16 v[136:139], v[72:75], v[92:95], v[136:139]
	v_mfma_f32_16x16x32_bf16 v[140:143], v[76:79], v[92:95], v[140:143]
	v_mfma_f32_16x16x32_bf16 v[144:147], v[80:83], v[92:95], v[144:147]
	v_mfma_f32_16x16x32_bf16 v[148:151], v[84:87], v[92:95], v[148:151]
	v_mfma_f32_16x16x32_bf16 v[152:155], v[72:75], v[96:99], v[152:155]
	v_mfma_f32_16x16x32_bf16 v[156:159], v[76:79], v[96:99], v[156:159]
	v_mfma_f32_16x16x32_bf16 v[160:163], v[80:83], v[96:99], v[160:163]
	v_mfma_f32_16x16x32_bf16 v[164:167], v[84:87], v[96:99], v[164:167]
	s_add_u32 s42, s41, 0x4000
	buffer_load_dwordx4 v[44:47], v1, s[4:7], s42 offen sc0 nt
	v_mfma_f32_16x16x32_bf16 v[168:171], v[72:75], v[100:103], v[168:171]
	v_mfma_f32_16x16x32_bf16 v[172:175], v[76:79], v[100:103], v[172:175]
	v_mfma_f32_16x16x32_bf16 v[176:179], v[80:83], v[100:103], v[176:179]
	v_mfma_f32_16x16x32_bf16 v[180:183], v[84:87], v[100:103], v[180:183]
	v_mfma_f32_16x16x32_bf16 v[184:187], v[72:75], v[104:107], v[184:187]
	v_mfma_f32_16x16x32_bf16 v[188:191], v[76:79], v[104:107], v[188:191]
	v_mfma_f32_16x16x32_bf16 v[192:195], v[80:83], v[104:107], v[192:195]
	v_mfma_f32_16x16x32_bf16 v[196:199], v[84:87], v[104:107], v[196:199]
	s_add_u32 s42, s41, 0x8000
	buffer_load_dwordx4 v[48:51], v1, s[4:7], s42 offen sc0 nt
	v_mfma_f32_16x16x32_bf16 v[200:203], v[72:75], v[108:111], v[200:203]
	v_mfma_f32_16x16x32_bf16 v[204:207], v[76:79], v[108:111], v[204:207]
	v_mfma_f32_16x16x32_bf16 v[208:211], v[80:83], v[108:111], v[208:211]
	v_mfma_f32_16x16x32_bf16 v[212:215], v[84:87], v[108:111], v[212:215]
	v_mfma_f32_16x16x32_bf16 v[216:219], v[72:75], v[112:115], v[216:219]
	v_mfma_f32_16x16x32_bf16 v[220:223], v[76:79], v[112:115], v[220:223]
	v_mfma_f32_16x16x32_bf16 v[224:227], v[80:83], v[112:115], v[224:227]
	v_mfma_f32_16x16x32_bf16 v[228:231], v[84:87], v[112:115], v[228:231]
	s_add_u32 s42, s41, 0xc000
	buffer_load_dwordx4 v[52:55], v1, s[4:7], s42 offen sc0 nt
	v_mfma_f32_16x16x32_bf16 v[232:235], v[72:75], v[116:119], v[232:235]
	v_mfma_f32_16x16x32_bf16 v[236:239], v[76:79], v[116:119], v[236:239]
	v_mfma_f32_16x16x32_bf16 v[240:243], v[80:83], v[116:119], v[240:243]
	v_mfma_f32_16x16x32_bf16 v[244:247], v[84:87], v[116:119], v[244:247]
	s_barrier
	ds_read_b128 v[72:75], v6 offset:1024
	ds_read_b128 v[76:79], v6 offset:3072
	ds_read_b128 v[80:83], v6 offset:5120
	ds_read_b128 v[84:87], v6 offset:7168
	ds_read_b128 v[88:91], v4 offset:1024
	ds_read_b128 v[92:95], v4 offset:3072
	ds_read_b128 v[96:99], v4 offset:5120
	ds_read_b128 v[100:103], v4 offset:7168
	ds_read_b128 v[104:107], v4 offset:9216
	ds_read_b128 v[108:111], v4 offset:11264
	ds_read_b128 v[112:115], v4 offset:13312
	ds_read_b128 v[116:119], v4 offset:15360
	s_waitcnt vmcnt(18)
	v_cvt_pk_bf16_f32 v56, v56, v57
	v_cvt_pk_bf16_f32 v57, v58, v59
	v_cvt_pk_bf16_f32 v60, v60, v61
	v_cvt_pk_bf16_f32 v61, v62, v63
	ds_write2st64_b64 v3, v[56:57], v[60:61] offset0:96 offset1:104
	s_waitcnt vmcnt(16)
	v_cvt_pk_bf16_f32 v64, v64, v65
	v_cvt_pk_bf16_f32 v65, v66, v67
	v_cvt_pk_bf16_f32 v68, v68, v69
	v_cvt_pk_bf16_f32 v69, v70, v71
	ds_write2st64_b64 v3, v[64:65], v[68:69] offset0:112 offset1:120
	s_waitcnt vmcnt(12)
	s_waitcnt lgkmcnt(0)
	s_barrier
	v_mfma_f32_16x16x32_bf16 v[120:123], v[72:75], v[88:91], v[120:123]
	s_add_u32 s33, s33, 0x8000
	s_cmp_eq_u32 s33, 0x18000
	s_cselect_b32 s33, 0, s33
	s_add_u32 s25, s25, 1
	s_mov_b32 m0, s26
	v_mfma_f32_16x16x32_bf16 v[124:127], v[76:79], v[88:91], v[124:127]
	buffer_load_dwordx4 v2, s[12:15], s44 offen sc1 lds
	v_mfma_f32_16x16x32_bf16 v[128:131], v[80:83], v[88:91], v[128:131]
	v_mfma_f32_16x16x32_bf16 v[132:135], v[84:87], v[88:91], v[132:135]
	v_mfma_f32_16x16x32_bf16 v[136:139], v[72:75], v[92:95], v[136:139]
	v_mfma_f32_16x16x32_bf16 v[140:143], v[76:79], v[92:95], v[140:143]
	s_add_u32 s42, s41, 0x10000
	buffer_load_dwordx4 v[56:59], v1, s[4:7], s42 offen sc0 nt
	v_mfma_f32_16x16x32_bf16 v[144:147], v[80:83], v[92:95], v[144:147]
	v_mfma_f32_16x16x32_bf16 v[148:151], v[84:87], v[92:95], v[148:151]
	v_mfma_f32_16x16x32_bf16 v[152:155], v[72:75], v[96:99], v[152:155]
	v_mfma_f32_16x16x32_bf16 v[156:159], v[76:79], v[96:99], v[156:159]
	buffer_load_dwordx4 v2, s[12:15], s44 offen offset:1024 sc1 lds
	v_mfma_f32_16x16x32_bf16 v[160:163], v[80:83], v[96:99], v[160:163]
	v_mfma_f32_16x16x32_bf16 v[164:167], v[84:87], v[96:99], v[164:167]
	v_mfma_f32_16x16x32_bf16 v[168:171], v[72:75], v[100:103], v[168:171]
	v_mfma_f32_16x16x32_bf16 v[172:175], v[76:79], v[100:103], v[172:175]
	s_add_u32 s42, s41, 0x14000
	buffer_load_dwordx4 v[60:63], v1, s[4:7], s42 offen sc0 nt
	v_mfma_f32_16x16x32_bf16 v[176:179], v[80:83], v[100:103], v[176:179]
	v_mfma_f32_16x16x32_bf16 v[180:183], v[84:87], v[100:103], v[180:183]
	v_mfma_f32_16x16x32_bf16 v[184:187], v[72:75], v[104:107], v[184:187]
	v_mfma_f32_16x16x32_bf16 v[188:191], v[76:79], v[104:107], v[188:191]
	buffer_load_dwordx4 v2, s[12:15], s44 offen offset:2048 sc1 lds
	v_mfma_f32_16x16x32_bf16 v[192:195], v[80:83], v[104:107], v[192:195]
	v_mfma_f32_16x16x32_bf16 v[196:199], v[84:87], v[104:107], v[196:199]
	v_mfma_f32_16x16x32_bf16 v[200:203], v[72:75], v[108:111], v[200:203]
	v_mfma_f32_16x16x32_bf16 v[204:207], v[76:79], v[108:111], v[204:207]
	s_add_u32 s42, s41, 0x18000
	buffer_load_dwordx4 v[64:67], v1, s[4:7], s42 offen sc0 nt
	v_mfma_f32_16x16x32_bf16 v[208:211], v[80:83], v[108:111], v[208:211]
	v_mfma_f32_16x16x32_bf16 v[212:215], v[84:87], v[108:111], v[212:215]
	v_mfma_f32_16x16x32_bf16 v[216:219], v[72:75], v[112:115], v[216:219]
	v_mfma_f32_16x16x32_bf16 v[220:223], v[76:79], v[112:115], v[220:223]
	buffer_load_dwordx4 v2, s[12:15], s44 offen offset:3072 sc1 lds
	v_mfma_f32_16x16x32_bf16 v[224:227], v[80:83], v[112:115], v[224:227]
	v_mfma_f32_16x16x32_bf16 v[228:231], v[84:87], v[112:115], v[228:231]
	v_mfma_f32_16x16x32_bf16 v[232:235], v[72:75], v[116:119], v[232:235]
	v_mfma_f32_16x16x32_bf16 v[236:239], v[76:79], v[116:119], v[236:239]
	s_add_u32 s42, s41, 0x1c000
	buffer_load_dwordx4 v[68:71], v1, s[4:7], s42 offen sc0 nt
	v_mfma_f32_16x16x32_bf16 v[240:243], v[80:83], v[116:119], v[240:243]
	s_add_u32 s26, s26, 0x8000
	s_cmp_eq_u32 s26, s32
	s_cselect_b32 s26, s27, s26
	v_mfma_f32_16x16x32_bf16 v[244:247], v[84:87], v[116:119], v[244:247]
	s_barrier
	v_add_u32_e32 v6, s33, v5
	ds_read_b128 v[72:75], v6 offset:0
	ds_read_b128 v[76:79], v6 offset:2048
	ds_read_b128 v[80:83], v6 offset:4096
	ds_read_b128 v[84:87], v6 offset:6144
	ds_read_b128 v[88:91], v4 offset:32768
	ds_read_b128 v[92:95], v4 offset:34816
	ds_read_b128 v[96:99], v4 offset:36864
	ds_read_b128 v[100:103], v4 offset:38912
	ds_read_b128 v[104:107], v4 offset:40960
	ds_read_b128 v[108:111], v4 offset:43008
	ds_read_b128 v[112:115], v4 offset:45056
	ds_read_b128 v[116:119], v4 offset:47104
	s_waitcnt vmcnt(18)
	v_cvt_pk_bf16_f32 v8, v8, v9
	v_cvt_pk_bf16_f32 v9, v10, v11
	v_cvt_pk_bf16_f32 v12, v12, v13
	v_cvt_pk_bf16_f32 v13, v14, v15
	ds_write2st64_b64 v3, v[8:9], v[12:13] offset0:0 offset1:8
	s_waitcnt vmcnt(16)
	v_cvt_pk_bf16_f32 v16, v16, v17
	v_cvt_pk_bf16_f32 v17, v18, v19
	v_cvt_pk_bf16_f32 v20, v20, v21
	v_cvt_pk_bf16_f32 v21, v22, v23
	ds_write2st64_b64 v3, v[16:17], v[20:21] offset0:16 offset1:24
	s_waitcnt lgkmcnt(0)
	s_barrier
	v_mfma_f32_16x16x32_bf16 v[120:123], v[72:75], v[88:91], v[120:123]
	s_min_u32 s40, s25, 31
	s_bitcmp1_b32 s40, 4
	s_cselect_b32 s41, s23, s22
	s_lshl_b32 s42, s40, 23
	s_and_b32 s42, s42, 0x7000000
	s_or_b32 s41, s41, s42
	s_lshl_b32 s42, s40, 8
	s_and_b32 s42, s42, 0x100
	s_or_b32 s41, s41, s42
	s_sub_u32 s43, s25, 1
	s_min_u32 s43, s43, 31
	s_and_b32 s43, s43, 15
	s_lshl_b32 s43, s43, 15
	s_add_u32 s44, s43, s24
	v_mfma_f32_16x16x32_bf16 v[124:127], v[76:79], v[88:91], v[124:127]
	v_mfma_f32_16x16x32_bf16 v[128:131], v[80:83], v[88:91], v[128:131]
	v_mfma_f32_16x16x32_bf16 v[132:135], v[84:87], v[88:91], v[132:135]
	buffer_load_dwordx4 v[8:11], v1, s[4:7], s41 offen sc0 nt
	v_mfma_f32_16x16x32_bf16 v[136:139], v[72:75], v[92:95], v[136:139]
	v_mfma_f32_16x16x32_bf16 v[140:143], v[76:79], v[92:95], v[140:143]
	v_mfma_f32_16x16x32_bf16 v[144:147], v[80:83], v[92:95], v[144:147]
	v_mfma_f32_16x16x32_bf16 v[148:151], v[84:87], v[92:95], v[148:151]
	v_mfma_f32_16x16x32_bf16 v[152:155], v[72:75], v[96:99], v[152:155]
	v_mfma_f32_16x16x32_bf16 v[156:159], v[76:79], v[96:99], v[156:159]
	v_mfma_f32_16x16x32_bf16 v[160:163], v[80:83], v[96:99], v[160:163]
	v_mfma_f32_16x16x32_bf16 v[164:167], v[84:87], v[96:99], v[164:167]
	s_add_u32 s42, s41, 0x4000
	buffer_load_dwordx4 v[12:15], v1, s[4:7], s42 offen sc0 nt
	v_mfma_f32_16x16x32_bf16 v[168:171], v[72:75], v[100:103], v[168:171]
	v_mfma_f32_16x16x32_bf16 v[172:175], v[76:79], v[100:103], v[172:175]
	v_mfma_f32_16x16x32_bf16 v[176:179], v[80:83], v[100:103], v[176:179]
	v_mfma_f32_16x16x32_bf16 v[180:183], v[84:87], v[100:103], v[180:183]
	v_mfma_f32_16x16x32_bf16 v[184:187], v[72:75], v[104:107], v[184:187]
	v_mfma_f32_16x16x32_bf16 v[188:191], v[76:79], v[104:107], v[188:191]
	v_mfma_f32_16x16x32_bf16 v[192:195], v[80:83], v[104:107], v[192:195]
	v_mfma_f32_16x16x32_bf16 v[196:199], v[84:87], v[104:107], v[196:199]
	s_add_u32 s42, s41, 0x8000
	buffer_load_dwordx4 v[16:19], v1, s[4:7], s42 offen sc0 nt
	v_mfma_f32_16x16x32_bf16 v[200:203], v[72:75], v[108:111], v[200:203]
	v_mfma_f32_16x16x32_bf16 v[204:207], v[76:79], v[108:111], v[204:207]
	v_mfma_f32_16x16x32_bf16 v[208:211], v[80:83], v[108:111], v[208:211]
	v_mfma_f32_16x16x32_bf16 v[212:215], v[84:87], v[108:111], v[212:215]
	v_mfma_f32_16x16x32_bf16 v[216:219], v[72:75], v[112:115], v[216:219]
	v_mfma_f32_16x16x32_bf16 v[220:223], v[76:79], v[112:115], v[220:223]
	v_mfma_f32_16x16x32_bf16 v[224:227], v[80:83], v[112:115], v[224:227]
	v_mfma_f32_16x16x32_bf16 v[228:231], v[84:87], v[112:115], v[228:231]
	s_add_u32 s42, s41, 0xc000
	buffer_load_dwordx4 v[20:23], v1, s[4:7], s42 offen sc0 nt
	v_mfma_f32_16x16x32_bf16 v[232:235], v[72:75], v[116:119], v[232:235]
	v_mfma_f32_16x16x32_bf16 v[236:239], v[76:79], v[116:119], v[236:239]
	v_mfma_f32_16x16x32_bf16 v[240:243], v[80:83], v[116:119], v[240:243]
	v_mfma_f32_16x16x32_bf16 v[244:247], v[84:87], v[116:119], v[244:247]
	s_barrier
	ds_read_b128 v[72:75], v6 offset:1024
	ds_read_b128 v[76:79], v6 offset:3072
	ds_read_b128 v[80:83], v6 offset:5120
	ds_read_b128 v[84:87], v6 offset:7168
	ds_read_b128 v[88:91], v4 offset:33792
	ds_read_b128 v[92:95], v4 offset:35840
	ds_read_b128 v[96:99], v4 offset:37888
	ds_read_b128 v[100:103], v4 offset:39936
	ds_read_b128 v[104:107], v4 offset:41984
	ds_read_b128 v[108:111], v4 offset:44032
	ds_read_b128 v[112:115], v4 offset:46080
	ds_read_b128 v[116:119], v4 offset:48128
	s_waitcnt vmcnt(18)
	v_cvt_pk_bf16_f32 v24, v24, v25
	v_cvt_pk_bf16_f32 v25, v26, v27
	v_cvt_pk_bf16_f32 v28, v28, v29
	v_cvt_pk_bf16_f32 v29, v30, v31
	ds_write2st64_b64 v3, v[24:25], v[28:29] offset0:32 offset1:40
	s_waitcnt vmcnt(16)
	v_cvt_pk_bf16_f32 v32, v32, v33
	v_cvt_pk_bf16_f32 v33, v34, v35
	v_cvt_pk_bf16_f32 v36, v36, v37
	v_cvt_pk_bf16_f32 v37, v38, v39
	ds_write2st64_b64 v3, v[32:33], v[36:37] offset0:48 offset1:56
	s_waitcnt vmcnt(5)
	s_waitcnt lgkmcnt(0)
	s_barrier
	v_mfma_f32_16x16x32_bf16 v[120:123], v[72:75], v[88:91], v[120:123]
	s_add_u32 s33, s33, 0x8000
	s_cmp_eq_u32 s33, 0x18000
	s_cselect_b32 s33, 0, s33
	s_add_u32 s25, s25, 1
	s_mov_b32 m0, s26
	v_mfma_f32_16x16x32_bf16 v[124:127], v[76:79], v[88:91], v[124:127]
	buffer_load_dwordx4 v2, s[12:15], s44 offen sc1 lds
	v_mfma_f32_16x16x32_bf16 v[128:131], v[80:83], v[88:91], v[128:131]
	v_mfma_f32_16x16x32_bf16 v[132:135], v[84:87], v[88:91], v[132:135]
	v_mfma_f32_16x16x32_bf16 v[136:139], v[72:75], v[92:95], v[136:139]
	v_mfma_f32_16x16x32_bf16 v[140:143], v[76:79], v[92:95], v[140:143]
	s_add_u32 s42, s41, 0x10000
	buffer_load_dwordx4 v[24:27], v1, s[4:7], s42 offen sc0 nt
	v_mfma_f32_16x16x32_bf16 v[144:147], v[80:83], v[92:95], v[144:147]
	v_mfma_f32_16x16x32_bf16 v[148:151], v[84:87], v[92:95], v[148:151]
	v_mfma_f32_16x16x32_bf16 v[152:155], v[72:75], v[96:99], v[152:155]
	v_mfma_f32_16x16x32_bf16 v[156:159], v[76:79], v[96:99], v[156:159]
	buffer_load_dwordx4 v2, s[12:15], s44 offen offset:1024 sc1 lds
	v_mfma_f32_16x16x32_bf16 v[160:163], v[80:83], v[96:99], v[160:163]
	v_mfma_f32_16x16x32_bf16 v[164:167], v[84:87], v[96:99], v[164:167]
	v_mfma_f32_16x16x32_bf16 v[168:171], v[72:75], v[100:103], v[168:171]
	v_mfma_f32_16x16x32_bf16 v[172:175], v[76:79], v[100:103], v[172:175]
	s_add_u32 s42, s41, 0x14000
	buffer_load_dwordx4 v[28:31], v1, s[4:7], s42 offen sc0 nt
	v_mfma_f32_16x16x32_bf16 v[176:179], v[80:83], v[100:103], v[176:179]
	v_mfma_f32_16x16x32_bf16 v[180:183], v[84:87], v[100:103], v[180:183]
	v_mfma_f32_16x16x32_bf16 v[184:187], v[72:75], v[104:107], v[184:187]
	v_mfma_f32_16x16x32_bf16 v[188:191], v[76:79], v[104:107], v[188:191]
	buffer_load_dwordx4 v2, s[12:15], s44 offen offset:2048 sc1 lds
	v_mfma_f32_16x16x32_bf16 v[192:195], v[80:83], v[104:107], v[192:195]
	v_mfma_f32_16x16x32_bf16 v[196:199], v[84:87], v[104:107], v[196:199]
	v_mfma_f32_16x16x32_bf16 v[200:203], v[72:75], v[108:111], v[200:203]
	v_mfma_f32_16x16x32_bf16 v[204:207], v[76:79], v[108:111], v[204:207]
	s_add_u32 s42, s41, 0x18000
	buffer_load_dwordx4 v[32:35], v1, s[4:7], s42 offen sc0 nt
	v_mfma_f32_16x16x32_bf16 v[208:211], v[80:83], v[108:111], v[208:211]
	v_mfma_f32_16x16x32_bf16 v[212:215], v[84:87], v[108:111], v[212:215]
	v_mfma_f32_16x16x32_bf16 v[216:219], v[72:75], v[112:115], v[216:219]
	v_mfma_f32_16x16x32_bf16 v[220:223], v[76:79], v[112:115], v[220:223]
	buffer_load_dwordx4 v2, s[12:15], s44 offen offset:3072 sc1 lds
	v_mfma_f32_16x16x32_bf16 v[224:227], v[80:83], v[112:115], v[224:227]
	v_mfma_f32_16x16x32_bf16 v[228:231], v[84:87], v[112:115], v[228:231]
	v_mfma_f32_16x16x32_bf16 v[232:235], v[72:75], v[116:119], v[232:235]
	v_mfma_f32_16x16x32_bf16 v[236:239], v[76:79], v[116:119], v[236:239]
	s_add_u32 s42, s41, 0x1c000
	buffer_load_dwordx4 v[36:39], v1, s[4:7], s42 offen sc0 nt
	v_mfma_f32_16x16x32_bf16 v[240:243], v[80:83], v[116:119], v[240:243]
	s_add_u32 s26, s26, 0x8000
	s_cmp_eq_u32 s26, s32
	s_cselect_b32 s26, s27, s26
	v_mfma_f32_16x16x32_bf16 v[244:247], v[84:87], v[116:119], v[244:247]
	s_barrier
	s_mov_b32 s38, 7
.Lg_loop0:
	v_add_u32_e32 v6, s33, v5
	ds_read_b128 v[72:75], v6 offset:0
	ds_read_b128 v[76:79], v6 offset:2048
	ds_read_b128 v[80:83], v6 offset:4096
	ds_read_b128 v[84:87], v6 offset:6144
	ds_read_b128 v[88:91], v4 offset:0
	ds_read_b128 v[92:95], v4 offset:2048
	ds_read_b128 v[96:99], v4 offset:4096
	ds_read_b128 v[100:103], v4 offset:6144
	ds_read_b128 v[104:107], v4 offset:8192
	ds_read_b128 v[108:111], v4 offset:10240
	ds_read_b128 v[112:115], v4 offset:12288
	ds_read_b128 v[116:119], v4 offset:14336
	s_waitcnt vmcnt(22)
	v_cvt_pk_bf16_f32 v40, v40, v41
	v_cvt_pk_bf16_f32 v41, v42, v43
	v_cvt_pk_bf16_f32 v44, v44, v45
	v_cvt_pk_bf16_f32 v45, v46, v47
	ds_write2st64_b64 v3, v[40:41], v[44:45] offset0:64 offset1:72
	s_waitcnt vmcnt(20)
	v_cvt_pk_bf16_f32 v48, v48, v49
	v_cvt_pk_bf16_f32 v49, v50, v51
	v_cvt_pk_bf16_f32 v52, v52, v53
	v_cvt_pk_bf16_f32 v53, v54, v55
	ds_write2st64_b64 v3, v[48:49], v[52:53] offset0:80 offset1:88
	s_waitcnt lgkmcnt(0)
	s_barrier
	v_mfma_f32_16x16x32_bf16 v[120:123], v[72:75], v[88:91], v[120:123]
	s_min_u32 s40, s25, 31
	s_bitcmp1_b32 s40, 4
	s_cselect_b32 s41, s23, s22
	s_lshl_b32 s42, s40, 23
	s_and_b32 s42, s42, 0x7000000
	s_or_b32 s41, s41, s42
	s_lshl_b32 s42, s40, 8
	s_and_b32 s42, s42, 0x100
	s_or_b32 s41, s41, s42
	s_sub_u32 s43, s25, 1
	s_min_u32 s43, s43, 31
	s_and_b32 s43, s43, 15
	s_lshl_b32 s43, s43, 15
	s_add_u32 s44, s43, s24
	v_mfma_f32_16x16x32_bf16 v[124:127], v[76:79], v[88:91], v[124:127]
	v_mfma_f32_16x16x32_bf16 v[128:131], v[80:83], v[88:91], v[128:131]
	v_mfma_f32_16x16x32_bf16 v[132:135], v[84:87], v[88:91], v[132:135]
	buffer_load_dwordx4 v[40:43], v1, s[4:7], s41 offen sc0 nt
	v_mfma_f32_16x16x32_bf16 v[136:139], v[72:75], v[92:95], v[136:139]
	v_mfma_f32_16x16x32_bf16 v[140:143], v[76:79], v[92:95], v[140:143]
	v_mfma_f32_16x16x32_bf16 v[144:147], v[80:83], v[92:95], v[144:147]
	v_mfma_f32_16x16x32_bf16 v[148:151], v[84:87], v[92:95], v[148:151]
	v_mfma_f32_16x16x32_bf16 v[152:155], v[72:75], v[96:99], v[152:155]
	v_mfma_f32_16x16x32_bf16 v[156:159], v[76:79], v[96:99], v[156:159]
	v_mfma_f32_16x16x32_bf16 v[160:163], v[80:83], v[96:99], v[160:163]
	v_mfma_f32_16x16x32_bf16 v[164:167], v[84:87], v[96:99], v[164:167]
	s_add_u32 s42, s41, 0x4000
	buffer_load_dwordx4 v[44:47], v1, s[4:7], s42 offen sc0 nt
	v_mfma_f32_16x16x32_bf16 v[168:171], v[72:75], v[100:103], v[168:171]
	v_mfma_f32_16x16x32_bf16 v[172:175], v[76:79], v[100:103], v[172:175]
	v_mfma_f32_16x16x32_bf16 v[176:179], v[80:83], v[100:103], v[176:179]
	v_mfma_f32_16x16x32_bf16 v[180:183], v[84:87], v[100:103], v[180:183]
	v_mfma_f32_16x16x32_bf16 v[184:187], v[72:75], v[104:107], v[184:187]
	v_mfma_f32_16x16x32_bf16 v[188:191], v[76:79], v[104:107], v[188:191]
	v_mfma_f32_16x16x32_bf16 v[192:195], v[80:83], v[104:107], v[192:195]
	v_mfma_f32_16x16x32_bf16 v[196:199], v[84:87], v[104:107], v[196:199]
	s_add_u32 s42, s41, 0x8000
	buffer_load_dwordx4 v[48:51], v1, s[4:7], s42 offen sc0 nt
	v_mfma_f32_16x16x32_bf16 v[200:203], v[72:75], v[108:111], v[200:203]
	v_mfma_f32_16x16x32_bf16 v[204:207], v[76:79], v[108:111], v[204:207]
	v_mfma_f32_16x16x32_bf16 v[208:211], v[80:83], v[108:111], v[208:211]
	v_mfma_f32_16x16x32_bf16 v[212:215], v[84:87], v[108:111], v[212:215]
	v_mfma_f32_16x16x32_bf16 v[216:219], v[72:75], v[112:115], v[216:219]
	v_mfma_f32_16x16x32_bf16 v[220:223], v[76:79], v[112:115], v[220:223]
	v_mfma_f32_16x16x32_bf16 v[224:227], v[80:83], v[112:115], v[224:227]
	v_mfma_f32_16x16x32_bf16 v[228:231], v[84:87], v[112:115], v[228:231]
	s_add_u32 s42, s41, 0xc000
	buffer_load_dwordx4 v[52:55], v1, s[4:7], s42 offen sc0 nt
	v_mfma_f32_16x16x32_bf16 v[232:235], v[72:75], v[116:119], v[232:235]
	v_mfma_f32_16x16x32_bf16 v[236:239], v[76:79], v[116:119], v[236:239]
	v_mfma_f32_16x16x32_bf16 v[240:243], v[80:83], v[116:119], v[240:243]
	v_mfma_f32_16x16x32_bf16 v[244:247], v[84:87], v[116:119], v[244:247]
	s_barrier
	ds_read_b128 v[72:75], v6 offset:1024
	ds_read_b128 v[76:79], v6 offset:3072
	ds_read_b128 v[80:83], v6 offset:5120
	ds_read_b128 v[84:87], v6 offset:7168
	ds_read_b128 v[88:91], v4 offset:1024
	ds_read_b128 v[92:95], v4 offset:3072
	ds_read_b128 v[96:99], v4 offset:5120
	ds_read_b128 v[100:103], v4 offset:7168
	ds_read_b128 v[104:107], v4 offset:9216
	ds_read_b128 v[108:111], v4 offset:11264
	ds_read_b128 v[112:115], v4 offset:13312
	ds_read_b128 v[116:119], v4 offset:15360
	s_waitcnt vmcnt(20)
	v_cvt_pk_bf16_f32 v56, v56, v57
	v_cvt_pk_bf16_f32 v57, v58, v59
	v_cvt_pk_bf16_f32 v60, v60, v61
	v_cvt_pk_bf16_f32 v61, v62, v63
	ds_write2st64_b64 v3, v[56:57], v[60:61] offset0:96 offset1:104
	s_waitcnt vmcnt(16)
	v_cvt_pk_bf16_f32 v64, v64, v65
	v_cvt_pk_bf16_f32 v65, v66, v67
	v_cvt_pk_bf16_f32 v68, v68, v69
	v_cvt_pk_bf16_f32 v69, v70, v71
	ds_write2st64_b64 v3, v[64:65], v[68:69] offset0:112 offset1:120
	s_waitcnt vmcnt(5)
	s_waitcnt lgkmcnt(0)
	s_barrier
	v_mfma_f32_16x16x32_bf16 v[120:123], v[72:75], v[88:91], v[120:123]
	s_add_u32 s33, s33, 0x8000
	s_cmp_eq_u32 s33, 0x18000
	s_cselect_b32 s33, 0, s33
	s_add_u32 s25, s25, 1
	s_mov_b32 m0, s26
	v_mfma_f32_16x16x32_bf16 v[124:127], v[76:79], v[88:91], v[124:127]
	buffer_load_dwordx4 v2, s[12:15], s44 offen sc1 lds
	v_mfma_f32_16x16x32_bf16 v[128:131], v[80:83], v[88:91], v[128:131]
	v_mfma_f32_16x16x32_bf16 v[132:135], v[84:87], v[88:91], v[132:135]
	v_mfma_f32_16x16x32_bf16 v[136:139], v[72:75], v[92:95], v[136:139]
	v_mfma_f32_16x16x32_bf16 v[140:143], v[76:79], v[92:95], v[140:143]
	s_add_u32 s42, s41, 0x10000
	buffer_load_dwordx4 v[56:59], v1, s[4:7], s42 offen sc0 nt
	v_mfma_f32_16x16x32_bf16 v[144:147], v[80:83], v[92:95], v[144:147]
	v_mfma_f32_16x16x32_bf16 v[148:151], v[84:87], v[92:95], v[148:151]
	v_mfma_f32_16x16x32_bf16 v[152:155], v[72:75], v[96:99], v[152:155]
	v_mfma_f32_16x16x32_bf16 v[156:159], v[76:79], v[96:99], v[156:159]
	buffer_load_dwordx4 v2, s[12:15], s44 offen offset:1024 sc1 lds
	v_mfma_f32_16x16x32_bf16 v[160:163], v[80:83], v[96:99], v[160:163]
	v_mfma_f32_16x16x32_bf16 v[164:167], v[84:87], v[96:99], v[164:167]
	v_mfma_f32_16x16x32_bf16 v[168:171], v[72:75], v[100:103], v[168:171]
	v_mfma_f32_16x16x32_bf16 v[172:175], v[76:79], v[100:103], v[172:175]
	s_add_u32 s42, s41, 0x14000
	buffer_load_dwordx4 v[60:63], v1, s[4:7], s42 offen sc0 nt
	v_mfma_f32_16x16x32_bf16 v[176:179], v[80:83], v[100:103], v[176:179]
	v_mfma_f32_16x16x32_bf16 v[180:183], v[84:87], v[100:103], v[180:183]
	v_mfma_f32_16x16x32_bf16 v[184:187], v[72:75], v[104:107], v[184:187]
	v_mfma_f32_16x16x32_bf16 v[188:191], v[76:79], v[104:107], v[188:191]
	buffer_load_dwordx4 v2, s[12:15], s44 offen offset:2048 sc1 lds
	v_mfma_f32_16x16x32_bf16 v[192:195], v[80:83], v[104:107], v[192:195]
	v_mfma_f32_16x16x32_bf16 v[196:199], v[84:87], v[104:107], v[196:199]
	v_mfma_f32_16x16x32_bf16 v[200:203], v[72:75], v[108:111], v[200:203]
	v_mfma_f32_16x16x32_bf16 v[204:207], v[76:79], v[108:111], v[204:207]
	s_add_u32 s42, s41, 0x18000
	buffer_load_dwordx4 v[64:67], v1, s[4:7], s42 offen sc0 nt
	v_mfma_f32_16x16x32_bf16 v[208:211], v[80:83], v[108:111], v[208:211]
	v_mfma_f32_16x16x32_bf16 v[212:215], v[84:87], v[108:111], v[212:215]
	v_mfma_f32_16x16x32_bf16 v[216:219], v[72:75], v[112:115], v[216:219]
	v_mfma_f32_16x16x32_bf16 v[220:223], v[76:79], v[112:115], v[220:223]
	buffer_load_dwordx4 v2, s[12:15], s44 offen offset:3072 sc1 lds
	v_mfma_f32_16x16x32_bf16 v[224:227], v[80:83], v[112:115], v[224:227]
	v_mfma_f32_16x16x32_bf16 v[228:231], v[84:87], v[112:115], v[228:231]
	v_mfma_f32_16x16x32_bf16 v[232:235], v[72:75], v[116:119], v[232:235]
	v_mfma_f32_16x16x32_bf16 v[236:239], v[76:79], v[116:119], v[236:239]
	s_add_u32 s42, s41, 0x1c000
	buffer_load_dwordx4 v[68:71], v1, s[4:7], s42 offen sc0 nt
	v_mfma_f32_16x16x32_bf16 v[240:243], v[80:83], v[116:119], v[240:243]
	s_add_u32 s26, s26, 0x8000
	s_cmp_eq_u32 s26, s32
	s_cselect_b32 s26, s27, s26
	v_mfma_f32_16x16x32_bf16 v[244:247], v[84:87], v[116:119], v[244:247]
	s_barrier
	v_add_u32_e32 v6, s33, v5
	ds_read_b128 v[72:75], v6 offset:0
	ds_read_b128 v[76:79], v6 offset:2048
	ds_read_b128 v[80:83], v6 offset:4096
	ds_read_b128 v[84:87], v6 offset:6144
	ds_read_b128 v[88:91], v4 offset:32768
	ds_read_b128 v[92:95], v4 offset:34816
	ds_read_b128 v[96:99], v4 offset:36864
	ds_read_b128 v[100:103], v4 offset:38912
	ds_read_b128 v[104:107], v4 offset:40960
	ds_read_b128 v[108:111], v4 offset:43008
	ds_read_b128 v[112:115], v4 offset:45056
	ds_read_b128 v[116:119], v4 offset:47104
	s_waitcnt vmcnt(22)
	v_cvt_pk_bf16_f32 v8, v8, v9
	v_cvt_pk_bf16_f32 v9, v10, v11
	v_cvt_pk_bf16_f32 v12, v12, v13
	v_cvt_pk_bf16_f32 v13, v14, v15
	ds_write2st64_b64 v3, v[8:9], v[12:13] offset0:0 offset1:8
	s_waitcnt vmcnt(20)
	v_cvt_pk_bf16_f32 v16, v16, v17
	v_cvt_pk_bf16_f32 v17, v18, v19
	v_cvt_pk_bf16_f32 v20, v20, v21
	v_cvt_pk_bf16_f32 v21, v22, v23
	ds_write2st64_b64 v3, v[16:17], v[20:21] offset0:16 offset1:24
	s_waitcnt lgkmcnt(0)
	s_barrier
	v_mfma_f32_16x16x32_bf16 v[120:123], v[72:75], v[88:91], v[120:123]
	s_min_u32 s40, s25, 31
	s_bitcmp1_b32 s40, 4
	s_cselect_b32 s41, s23, s22
	s_lshl_b32 s42, s40, 23
	s_and_b32 s42, s42, 0x7000000
	s_or_b32 s41, s41, s42
	s_lshl_b32 s42, s40, 8
	s_and_b32 s42, s42, 0x100
	s_or_b32 s41, s41, s42
	s_sub_u32 s43, s25, 1
	s_min_u32 s43, s43, 31
	s_and_b32 s43, s43, 15
	s_lshl_b32 s43, s43, 15
	s_add_u32 s44, s43, s24
	v_mfma_f32_16x16x32_bf16 v[124:127], v[76:79], v[88:91], v[124:127]
	v_mfma_f32_16x16x32_bf16 v[128:131], v[80:83], v[88:91], v[128:131]
	v_mfma_f32_16x16x32_bf16 v[132:135], v[84:87], v[88:91], v[132:135]
	buffer_load_dwordx4 v[8:11], v1, s[4:7], s41 offen sc0 nt
	v_mfma_f32_16x16x32_bf16 v[136:139], v[72:75], v[92:95], v[136:139]
	v_mfma_f32_16x16x32_bf16 v[140:143], v[76:79], v[92:95], v[140:143]
	v_mfma_f32_16x16x32_bf16 v[144:147], v[80:83], v[92:95], v[144:147]
	v_mfma_f32_16x16x32_bf16 v[148:151], v[84:87], v[92:95], v[148:151]
	v_mfma_f32_16x16x32_bf16 v[152:155], v[72:75], v[96:99], v[152:155]
	v_mfma_f32_16x16x32_bf16 v[156:159], v[76:79], v[96:99], v[156:159]
	v_mfma_f32_16x16x32_bf16 v[160:163], v[80:83], v[96:99], v[160:163]
	v_mfma_f32_16x16x32_bf16 v[164:167], v[84:87], v[96:99], v[164:167]
	s_add_u32 s42, s41, 0x4000
	buffer_load_dwordx4 v[12:15], v1, s[4:7], s42 offen sc0 nt
	v_mfma_f32_16x16x32_bf16 v[168:171], v[72:75], v[100:103], v[168:171]
	v_mfma_f32_16x16x32_bf16 v[172:175], v[76:79], v[100:103], v[172:175]
	v_mfma_f32_16x16x32_bf16 v[176:179], v[80:83], v[100:103], v[176:179]
	v_mfma_f32_16x16x32_bf16 v[180:183], v[84:87], v[100:103], v[180:183]
	v_mfma_f32_16x16x32_bf16 v[184:187], v[72:75], v[104:107], v[184:187]
	v_mfma_f32_16x16x32_bf16 v[188:191], v[76:79], v[104:107], v[188:191]
	v_mfma_f32_16x16x32_bf16 v[192:195], v[80:83], v[104:107], v[192:195]
	v_mfma_f32_16x16x32_bf16 v[196:199], v[84:87], v[104:107], v[196:199]
	s_add_u32 s42, s41, 0x8000
	buffer_load_dwordx4 v[16:19], v1, s[4:7], s42 offen sc0 nt
	v_mfma_f32_16x16x32_bf16 v[200:203], v[72:75], v[108:111], v[200:203]
	v_mfma_f32_16x16x32_bf16 v[204:207], v[76:79], v[108:111], v[204:207]
	v_mfma_f32_16x16x32_bf16 v[208:211], v[80:83], v[108:111], v[208:211]
	v_mfma_f32_16x16x32_bf16 v[212:215], v[84:87], v[108:111], v[212:215]
	v_mfma_f32_16x16x32_bf16 v[216:219], v[72:75], v[112:115], v[216:219]
	v_mfma_f32_16x16x32_bf16 v[220:223], v[76:79], v[112:115], v[220:223]
	v_mfma_f32_16x16x32_bf16 v[224:227], v[80:83], v[112:115], v[224:227]
	v_mfma_f32_16x16x32_bf16 v[228:231], v[84:87], v[112:115], v[228:231]
	s_add_u32 s42, s41, 0xc000
	buffer_load_dwordx4 v[20:23], v1, s[4:7], s42 offen sc0 nt
	v_mfma_f32_16x16x32_bf16 v[232:235], v[72:75], v[116:119], v[232:235]
	v_mfma_f32_16x16x32_bf16 v[236:239], v[76:79], v[116:119], v[236:239]
	v_mfma_f32_16x16x32_bf16 v[240:243], v[80:83], v[116:119], v[240:243]
	v_mfma_f32_16x16x32_bf16 v[244:247], v[84:87], v[116:119], v[244:247]
	s_barrier
	ds_read_b128 v[72:75], v6 offset:1024
	ds_read_b128 v[76:79], v6 offset:3072
	ds_read_b128 v[80:83], v6 offset:5120
	ds_read_b128 v[84:87], v6 offset:7168
	ds_read_b128 v[88:91], v4 offset:33792
	ds_read_b128 v[92:95], v4 offset:35840
	ds_read_b128 v[96:99], v4 offset:37888
	ds_read_b128 v[100:103], v4 offset:39936
	ds_read_b128 v[104:107], v4 offset:41984
	ds_read_b128 v[108:111], v4 offset:44032
	ds_read_b128 v[112:115], v4 offset:46080
	ds_read_b128 v[116:119], v4 offset:48128
	s_waitcnt vmcnt(20)
	v_cvt_pk_bf16_f32 v24, v24, v25
	v_cvt_pk_bf16_f32 v25, v26, v27
	v_cvt_pk_bf16_f32 v28, v28, v29
	v_cvt_pk_bf16_f32 v29, v30, v31
	ds_write2st64_b64 v3, v[24:25], v[28:29] offset0:32 offset1:40
	s_waitcnt vmcnt(16)
	v_cvt_pk_bf16_f32 v32, v32, v33
	v_cvt_pk_bf16_f32 v33, v34, v35
	v_cvt_pk_bf16_f32 v36, v36, v37
	v_cvt_pk_bf16_f32 v37, v38, v39
	ds_write2st64_b64 v3, v[32:33], v[36:37] offset0:48 offset1:56
	s_waitcnt vmcnt(5)
	s_waitcnt lgkmcnt(0)
	s_barrier
	v_mfma_f32_16x16x32_bf16 v[120:123], v[72:75], v[88:91], v[120:123]
	s_add_u32 s33, s33, 0x8000
	s_cmp_eq_u32 s33, 0x18000
	s_cselect_b32 s33, 0, s33
	s_add_u32 s25, s25, 1
	s_mov_b32 m0, s26
	v_mfma_f32_16x16x32_bf16 v[124:127], v[76:79], v[88:91], v[124:127]
	buffer_load_dwordx4 v2, s[12:15], s44 offen sc1 lds
	v_mfma_f32_16x16x32_bf16 v[128:131], v[80:83], v[88:91], v[128:131]
	v_mfma_f32_16x16x32_bf16 v[132:135], v[84:87], v[88:91], v[132:135]
	v_mfma_f32_16x16x32_bf16 v[136:139], v[72:75], v[92:95], v[136:139]
	v_mfma_f32_16x16x32_bf16 v[140:143], v[76:79], v[92:95], v[140:143]
	s_add_u32 s42, s41, 0x10000
	buffer_load_dwordx4 v[24:27], v1, s[4:7], s42 offen sc0 nt
	v_mfma_f32_16x16x32_bf16 v[144:147], v[80:83], v[92:95], v[144:147]
	v_mfma_f32_16x16x32_bf16 v[148:151], v[84:87], v[92:95], v[148:151]
	v_mfma_f32_16x16x32_bf16 v[152:155], v[72:75], v[96:99], v[152:155]
	v_mfma_f32_16x16x32_bf16 v[156:159], v[76:79], v[96:99], v[156:159]
	buffer_load_dwordx4 v2, s[12:15], s44 offen offset:1024 sc1 lds
	v_mfma_f32_16x16x32_bf16 v[160:163], v[80:83], v[96:99], v[160:163]
	v_mfma_f32_16x16x32_bf16 v[164:167], v[84:87], v[96:99], v[164:167]
	v_mfma_f32_16x16x32_bf16 v[168:171], v[72:75], v[100:103], v[168:171]
	v_mfma_f32_16x16x32_bf16 v[172:175], v[76:79], v[100:103], v[172:175]
	s_add_u32 s42, s41, 0x14000
	buffer_load_dwordx4 v[28:31], v1, s[4:7], s42 offen sc0 nt
	v_mfma_f32_16x16x32_bf16 v[176:179], v[80:83], v[100:103], v[176:179]
	v_mfma_f32_16x16x32_bf16 v[180:183], v[84:87], v[100:103], v[180:183]
	v_mfma_f32_16x16x32_bf16 v[184:187], v[72:75], v[104:107], v[184:187]
	v_mfma_f32_16x16x32_bf16 v[188:191], v[76:79], v[104:107], v[188:191]
	buffer_load_dwordx4 v2, s[12:15], s44 offen offset:2048 sc1 lds
	v_mfma_f32_16x16x32_bf16 v[192:195], v[80:83], v[104:107], v[192:195]
	v_mfma_f32_16x16x32_bf16 v[196:199], v[84:87], v[104:107], v[196:199]
	v_mfma_f32_16x16x32_bf16 v[200:203], v[72:75], v[108:111], v[200:203]
	v_mfma_f32_16x16x32_bf16 v[204:207], v[76:79], v[108:111], v[204:207]
	s_add_u32 s42, s41, 0x18000
	buffer_load_dwordx4 v[32:35], v1, s[4:7], s42 offen sc0 nt
	v_mfma_f32_16x16x32_bf16 v[208:211], v[80:83], v[108:111], v[208:211]
	v_mfma_f32_16x16x32_bf16 v[212:215], v[84:87], v[108:111], v[212:215]
	v_mfma_f32_16x16x32_bf16 v[216:219], v[72:75], v[112:115], v[216:219]
	v_mfma_f32_16x16x32_bf16 v[220:223], v[76:79], v[112:115], v[220:223]
	buffer_load_dwordx4 v2, s[12:15], s44 offen offset:3072 sc1 lds
	v_mfma_f32_16x16x32_bf16 v[224:227], v[80:83], v[112:115], v[224:227]
	v_mfma_f32_16x16x32_bf16 v[228:231], v[84:87], v[112:115], v[228:231]
	v_mfma_f32_16x16x32_bf16 v[232:235], v[72:75], v[116:119], v[232:235]
	v_mfma_f32_16x16x32_bf16 v[236:239], v[76:79], v[116:119], v[236:239]
	s_add_u32 s42, s41, 0x1c000
	buffer_load_dwordx4 v[36:39], v1, s[4:7], s42 offen sc0 nt
	v_mfma_f32_16x16x32_bf16 v[240:243], v[80:83], v[116:119], v[240:243]
	s_add_u32 s26, s26, 0x8000
	s_cmp_eq_u32 s26, s32
	s_cselect_b32 s26, s27, s26
	v_mfma_f32_16x16x32_bf16 v[244:247], v[84:87], v[116:119], v[244:247]
	s_barrier
	s_sub_u32 s38, s38, 1
	s_cmp_lg_u32 s38, 0
	s_cbranch_scc1 .Lg_loop0
	v_add_u32_e32 v6, s33, v5
	ds_read_b128 v[72:75], v6 offset:0
	ds_read_b128 v[76:79], v6 offset:2048
	ds_read_b128 v[80:83], v6 offset:4096
	ds_read_b128 v[84:87], v6 offset:6144
	ds_read_b128 v[88:91], v4 offset:0
	ds_read_b128 v[92:95], v4 offset:2048
	ds_read_b128 v[96:99], v4 offset:4096
	ds_read_b128 v[100:103], v4 offset:6144
	ds_read_b128 v[104:107], v4 offset:8192
	ds_read_b128 v[108:111], v4 offset:10240
	ds_read_b128 v[112:115], v4 offset:12288
	ds_read_b128 v[116:119], v4 offset:14336
	s_waitcnt vmcnt(22)
	v_cvt_pk_bf16_f32 v40, v40, v41
	v_cvt_pk_bf16_f32 v41, v42, v43
	v_cvt_pk_bf16_f32 v44, v44, v45
	v_cvt_pk_bf16_f32 v45, v46, v47
	ds_write2st64_b64 v3, v[40:41], v[44:45] offset0:64 offset1:72
	s_waitcnt vmcnt(20)
	v_cvt_pk_bf16_f32 v48, v48, v49
	v_cvt_pk_bf16_f32 v49, v50, v51
	v_cvt_pk_bf16_f32 v52, v52, v53
	v_cvt_pk_bf16_f32 v53, v54, v55
	ds_write2st64_b64 v3, v[48:49], v[52:53] offset0:80 offset1:88
	s_waitcnt lgkmcnt(0)
	global_load_dwordx4 v[40:43], v249, s[34:35] offset:0
	global_load_dwordx4 v[44:47], v249, s[34:35] offset:64
	global_load_dwordx4 v[48:51], v249, s[34:35] offset:128
	global_load_dwordx4 v[52:55], v249, s[34:35] offset:192
	s_barrier
	s_mov_b32 m0, s26
	s_min_u32 s40, s25, 31
	s_bitcmp1_b32 s40, 4
	s_cselect_b32 s41, s23, s22
	s_lshl_b32 s42, s40, 23
	s_and_b32 s42, s42, 0x7000000
	s_or_b32 s41, s41, s42
	s_lshl_b32 s42, s40, 8
	s_and_b32 s42, s42, 0x100
	s_or_b32 s41, s41, s42
	s_sub_u32 s43, s25, 1
	s_min_u32 s43, s43, 31
	s_and_b32 s43, s43, 15
	s_lshl_b32 s43, s43, 15
	s_add_u32 s44, s43, s24
	buffer_load_dwordx4 v2, s[12:15], s44 offen sc1 lds
	buffer_load_dwordx4 v2, s[12:15], s44 offen offset:1024 sc1 lds
	buffer_load_dwordx4 v2, s[12:15], s44 offen offset:2048 sc1 lds
	buffer_load_dwordx4 v2, s[12:15], s44 offen offset:3072 sc1 lds
	s_waitcnt vmcnt(4)
	s_mov_b32 s45, s36
	buffer_store_dwordx4 v[120:123], v248, s[28:31], s45 offen
	buffer_store_dwordx4 v[124:127], v248, s[28:31], s45 offen offset:64
	v_mfma_f32_16x16x32_bf16 v[120:123], v[72:75], v[88:91], v[40:43]
	buffer_store_dwordx4 v[128:131], v248, s[28:31], s45 offen offset:128
	v_mfma_f32_16x16x32_bf16 v[124:127], v[76:79], v[88:91], v[44:47]
	buffer_store_dwordx4 v[132:135], v248, s[28:31], s45 offen offset:192
	v_mfma_f32_16x16x32_bf16 v[128:131], v[80:83], v[88:91], v[48:51]
	s_add_u32 s45, s36, 0x2000
	buffer_store_dwordx4 v[136:139], v248, s[28:31], s45 offen
	v_mfma_f32_16x16x32_bf16 v[132:135], v[84:87], v[88:91], v[52:55]
	buffer_store_dwordx4 v[140:143], v248, s[28:31], s45 offen offset:64
	v_mfma_f32_16x16x32_bf16 v[136:139], v[72:75], v[92:95], v[40:43]
	buffer_store_dwordx4 v[144:147], v248, s[28:31], s45 offen offset:128
	v_mfma_f32_16x16x32_bf16 v[140:143], v[76:79], v[92:95], v[44:47]
	buffer_store_dwordx4 v[148:151], v248, s[28:31], s45 offen offset:192
	v_mfma_f32_16x16x32_bf16 v[144:147], v[80:83], v[92:95], v[48:51]
	s_add_u32 s45, s36, 0x4000
	buffer_store_dwordx4 v[152:155], v248, s[28:31], s45 offen
	v_mfma_f32_16x16x32_bf16 v[148:151], v[84:87], v[92:95], v[52:55]
	buffer_store_dwordx4 v[156:159], v248, s[28:31], s45 offen offset:64
	v_mfma_f32_16x16x32_bf16 v[152:155], v[72:75], v[96:99], v[40:43]
	buffer_store_dwordx4 v[160:163], v248, s[28:31], s45 offen offset:128
	v_mfma_f32_16x16x32_bf16 v[156:159], v[76:79], v[96:99], v[44:47]
	buffer_store_dwordx4 v[164:167], v248, s[28:31], s45 offen offset:192
	v_mfma_f32_16x16x32_bf16 v[160:163], v[80:83], v[96:99], v[48:51]
	s_add_u32 s45, s36, 0x6000
	buffer_store_dwordx4 v[168:171], v248, s[28:31], s45 offen
	v_mfma_f32_16x16x32_bf16 v[164:167], v[84:87], v[96:99], v[52:55]
	buffer_store_dwordx4 v[172:175], v248, s[28:31], s45 offen offset:64
	v_mfma_f32_16x16x32_bf16 v[168:171], v[72:75], v[100:103], v[40:43]
	buffer_store_dwordx4 v[176:179], v248, s[28:31], s45 offen offset:128
	v_mfma_f32_16x16x32_bf16 v[172:175], v[76:79], v[100:103], v[44:47]
	buffer_store_dwordx4 v[180:183], v248, s[28:31], s45 offen offset:192
	v_mfma_f32_16x16x32_bf16 v[176:179], v[80:83], v[100:103], v[48:51]
	s_add_u32 s45, s36, 0x8000
	buffer_store_dwordx4 v[184:187], v248, s[28:31], s45 offen
	v_mfma_f32_16x16x32_bf16 v[180:183], v[84:87], v[100:103], v[52:55]
	buffer_store_dwordx4 v[188:191], v248, s[28:31], s45 offen offset:64
	v_mfma_f32_16x16x32_bf16 v[184:187], v[72:75], v[104:107], v[40:43]
	buffer_store_dwordx4 v[192:195], v248, s[28:31], s45 offen offset:128
	v_mfma_f32_16x16x32_bf16 v[188:191], v[76:79], v[104:107], v[44:47]
	buffer_store_dwordx4 v[196:199], v248, s[28:31], s45 offen offset:192
	v_mfma_f32_16x16x32_bf16 v[192:195], v[80:83], v[104:107], v[48:51]
	s_add_u32 s45, s36, 0xa000
	buffer_store_dwordx4 v[200:203], v248, s[28:31], s45 offen
	v_mfma_f32_16x16x32_bf16 v[196:199], v[84:87], v[104:107], v[52:55]
	buffer_store_dwordx4 v[204:207], v248, s[28:31], s45 offen offset:64
	v_mfma_f32_16x16x32_bf16 v[200:203], v[72:75], v[108:111], v[40:43]
	buffer_store_dwordx4 v[208:211], v248, s[28:31], s45 offen offset:128
	v_mfma_f32_16x16x32_bf16 v[204:207], v[76:79], v[108:111], v[44:47]
	buffer_store_dwordx4 v[212:215], v248, s[28:31], s45 offen offset:192
	v_mfma_f32_16x16x32_bf16 v[208:211], v[80:83], v[108:111], v[48:51]
	s_add_u32 s45, s36, 0xc000
	buffer_store_dwordx4 v[216:219], v248, s[28:31], s45 offen
	v_mfma_f32_16x16x32_bf16 v[212:215], v[84:87], v[108:111], v[52:55]
	buffer_store_dwordx4 v[220:223], v248, s[28:31], s45 offen offset:64
	v_mfma_f32_16x16x32_bf16 v[216:219], v[72:75], v[112:115], v[40:43]
	buffer_store_dwordx4 v[224:227], v248, s[28:31], s45 offen offset:128
	v_mfma_f32_16x16x32_bf16 v[220:223], v[76:79], v[112:115], v[44:47]
	buffer_store_dwordx4 v[228:231], v248, s[28:31], s45 offen offset:192
	v_mfma_f32_16x16x32_bf16 v[224:227], v[80:83], v[112:115], v[48:51]
	s_add_u32 s45, s36, 0xe000
	buffer_store_dwordx4 v[232:235], v248, s[28:31], s45 offen
	v_mfma_f32_16x16x32_bf16 v[228:231], v[84:87], v[112:115], v[52:55]
	buffer_store_dwordx4 v[236:239], v248, s[28:31], s45 offen offset:64
	v_mfma_f32_16x16x32_bf16 v[232:235], v[72:75], v[116:119], v[40:43]
	buffer_store_dwordx4 v[240:243], v248, s[28:31], s45 offen offset:128
	v_mfma_f32_16x16x32_bf16 v[236:239], v[76:79], v[116:119], v[44:47]
	buffer_store_dwordx4 v[244:247], v248, s[28:31], s45 offen offset:192
	v_mfma_f32_16x16x32_bf16 v[240:243], v[80:83], v[116:119], v[48:51]
	v_mfma_f32_16x16x32_bf16 v[244:247], v[84:87], v[116:119], v[52:55]
	s_barrier
	ds_read_b128 v[72:75], v6 offset:1024
	ds_read_b128 v[76:79], v6 offset:3072
	ds_read_b128 v[80:83], v6 offset:5120
	ds_read_b128 v[84:87], v6 offset:7168
	ds_read_b128 v[88:91], v4 offset:1024
	ds_read_b128 v[92:95], v4 offset:3072
	ds_read_b128 v[96:99], v4 offset:5120
	ds_read_b128 v[100:103], v4 offset:7168
	ds_read_b128 v[104:107], v4 offset:9216
	ds_read_b128 v[108:111], v4 offset:11264
	ds_read_b128 v[112:115], v4 offset:13312
	ds_read_b128 v[116:119], v4 offset:15360
	s_waitcnt vmcnt(56)
	v_cvt_pk_bf16_f32 v56, v56, v57
	v_cvt_pk_bf16_f32 v57, v58, v59
	v_cvt_pk_bf16_f32 v60, v60, v61
	v_cvt_pk_bf16_f32 v61, v62, v63
	ds_write2st64_b64 v3, v[56:57], v[60:61] offset0:96 offset1:104
	s_waitcnt vmcnt(52)
	v_cvt_pk_bf16_f32 v64, v64, v65
	v_cvt_pk_bf16_f32 v65, v66, v67
	v_cvt_pk_bf16_f32 v68, v68, v69
	v_cvt_pk_bf16_f32 v69, v70, v71
	ds_write2st64_b64 v3, v[64:65], v[68:69] offset0:112 offset1:120
	s_waitcnt vmcnt(41)
	s_waitcnt lgkmcnt(0)
	s_barrier
	v_mfma_f32_16x16x32_bf16 v[120:123], v[72:75], v[88:91], v[120:123]
	s_add_u32 s33, s33, 0x8000
	s_cmp_eq_u32 s33, 0x18000
	s_cselect_b32 s33, 0, s33
	s_add_u32 s25, s25, 1
	v_mfma_f32_16x16x32_bf16 v[124:127], v[76:79], v[88:91], v[124:127]
	v_mfma_f32_16x16x32_bf16 v[128:131], v[80:83], v[88:91], v[128:131]
	buffer_load_dwordx4 v[40:43], v1, s[4:7], s41 offen sc0 nt
	v_mfma_f32_16x16x32_bf16 v[132:135], v[84:87], v[88:91], v[132:135]
	v_mfma_f32_16x16x32_bf16 v[136:139], v[72:75], v[92:95], v[136:139]
	v_mfma_f32_16x16x32_bf16 v[140:143], v[76:79], v[92:95], v[140:143]
	v_mfma_f32_16x16x32_bf16 v[144:147], v[80:83], v[92:95], v[144:147]
	s_add_u32 s42, s41, 0x4000
	buffer_load_dwordx4 v[44:47], v1, s[4:7], s42 offen sc0 nt
	v_mfma_f32_16x16x32_bf16 v[148:151], v[84:87], v[92:95], v[148:151]
	v_mfma_f32_16x16x32_bf16 v[152:155], v[72:75], v[96:99], v[152:155]
	v_mfma_f32_16x16x32_bf16 v[156:159], v[76:79], v[96:99], v[156:159]
	v_mfma_f32_16x16x32_bf16 v[160:163], v[80:83], v[96:99], v[160:163]
	s_add_u32 s42, s41, 0x8000
	buffer_load_dwordx4 v[48:51], v1, s[4:7], s42 offen sc0 nt
	v_mfma_f32_16x16x32_bf16 v[164:167], v[84:87], v[96:99], v[164:167]
	v_mfma_f32_16x16x32_bf16 v[168:171], v[72:75], v[100:103], v[168:171]
	v_mfma_f32_16x16x32_bf16 v[172:175], v[76:79], v[100:103], v[172:175]
	v_mfma_f32_16x16x32_bf16 v[176:179], v[80:83], v[100:103], v[176:179]
	s_add_u32 s42, s41, 0xc000
	buffer_load_dwordx4 v[52:55], v1, s[4:7], s42 offen sc0 nt
	v_mfma_f32_16x16x32_bf16 v[180:183], v[84:87], v[100:103], v[180:183]
	v_mfma_f32_16x16x32_bf16 v[184:187], v[72:75], v[104:107], v[184:187]
	v_mfma_f32_16x16x32_bf16 v[188:191], v[76:79], v[104:107], v[188:191]
	v_mfma_f32_16x16x32_bf16 v[192:195], v[80:83], v[104:107], v[192:195]
	s_add_u32 s42, s41, 0x10000
	buffer_load_dwordx4 v[56:59], v1, s[4:7], s42 offen sc0 nt
	v_mfma_f32_16x16x32_bf16 v[196:199], v[84:87], v[104:107], v[196:199]
	v_mfma_f32_16x16x32_bf16 v[200:203], v[72:75], v[108:111], v[200:203]
	v_mfma_f32_16x16x32_bf16 v[204:207], v[76:79], v[108:111], v[204:207]
	v_mfma_f32_16x16x32_bf16 v[208:211], v[80:83], v[108:111], v[208:211]
	s_add_u32 s42, s41, 0x14000
	buffer_load_dwordx4 v[60:63], v1, s[4:7], s42 offen sc0 nt
	v_mfma_f32_16x16x32_bf16 v[212:215], v[84:87], v[108:111], v[212:215]
	v_mfma_f32_16x16x32_bf16 v[216:219], v[72:75], v[112:115], v[216:219]
	v_mfma_f32_16x16x32_bf16 v[220:223], v[76:79], v[112:115], v[220:223]
	v_mfma_f32_16x16x32_bf16 v[224:227], v[80:83], v[112:115], v[224:227]
	s_add_u32 s42, s41, 0x18000
	buffer_load_dwordx4 v[64:67], v1, s[4:7], s42 offen sc0 nt
	v_mfma_f32_16x16x32_bf16 v[228:231], v[84:87], v[112:115], v[228:231]
	v_mfma_f32_16x16x32_bf16 v[232:235], v[72:75], v[116:119], v[232:235]
	v_mfma_f32_16x16x32_bf16 v[236:239], v[76:79], v[116:119], v[236:239]
	v_mfma_f32_16x16x32_bf16 v[240:243], v[80:83], v[116:119], v[240:243]
	s_add_u32 s42, s41, 0x1c000
	buffer_load_dwordx4 v[68:71], v1, s[4:7], s42 offen sc0 nt
	s_add_u32 s26, s26, 0x8000
	s_cmp_eq_u32 s26, s32
	s_cselect_b32 s26, s27, s26
	v_mfma_f32_16x16x32_bf16 v[244:247], v[84:87], v[116:119], v[244:247]
	s_barrier
	v_add_u32_e32 v6, s33, v5
	ds_read_b128 v[72:75], v6 offset:0
	ds_read_b128 v[76:79], v6 offset:2048
	ds_read_b128 v[80:83], v6 offset:4096
	ds_read_b128 v[84:87], v6 offset:6144
	ds_read_b128 v[88:91], v4 offset:32768
	ds_read_b128 v[92:95], v4 offset:34816
	ds_read_b128 v[96:99], v4 offset:36864
	ds_read_b128 v[100:103], v4 offset:38912
	ds_read_b128 v[104:107], v4 offset:40960
	ds_read_b128 v[108:111], v4 offset:43008
	ds_read_b128 v[112:115], v4 offset:45056
	ds_read_b128 v[116:119], v4 offset:47104
	s_waitcnt vmcnt(58)
	v_cvt_pk_bf16_f32 v8, v8, v9
	v_cvt_pk_bf16_f32 v9, v10, v11
	v_cvt_pk_bf16_f32 v12, v12, v13
	v_cvt_pk_bf16_f32 v13, v14, v15
	ds_write2st64_b64 v3, v[8:9], v[12:13] offset0:0 offset1:8
	s_waitcnt vmcnt(56)
	v_cvt_pk_bf16_f32 v16, v16, v17
	v_cvt_pk_bf16_f32 v17, v18, v19
	v_cvt_pk_bf16_f32 v20, v20, v21
	v_cvt_pk_bf16_f32 v21, v22, v23
	ds_write2st64_b64 v3, v[16:17], v[20:21] offset0:16 offset1:24
	s_waitcnt lgkmcnt(0)
	s_barrier
	v_mfma_f32_16x16x32_bf16 v[120:123], v[72:75], v[88:91], v[120:123]
	s_min_u32 s40, s25, 31
	s_bitcmp1_b32 s40, 4
	s_cselect_b32 s41, s23, s22
	s_lshl_b32 s42, s40, 23
	s_and_b32 s42, s42, 0x7000000
	s_or_b32 s41, s41, s42
	s_lshl_b32 s42, s40, 8
	s_and_b32 s42, s42, 0x100
	s_or_b32 s41, s41, s42
	s_sub_u32 s43, s25, 1
	s_min_u32 s43, s43, 31
	s_and_b32 s43, s43, 15
	s_lshl_b32 s43, s43, 15
	s_add_u32 s44, s43, s24
	v_mfma_f32_16x16x32_bf16 v[124:127], v[76:79], v[88:91], v[124:127]
	v_mfma_f32_16x16x32_bf16 v[128:131], v[80:83], v[88:91], v[128:131]
	v_mfma_f32_16x16x32_bf16 v[132:135], v[84:87], v[88:91], v[132:135]
	buffer_load_dwordx4 v[8:11], v1, s[4:7], s41 offen sc0 nt
	v_mfma_f32_16x16x32_bf16 v[136:139], v[72:75], v[92:95], v[136:139]
	v_mfma_f32_16x16x32_bf16 v[140:143], v[76:79], v[92:95], v[140:143]
	v_mfma_f32_16x16x32_bf16 v[144:147], v[80:83], v[92:95], v[144:147]
	v_mfma_f32_16x16x32_bf16 v[148:151], v[84:87], v[92:95], v[148:151]
	v_mfma_f32_16x16x32_bf16 v[152:155], v[72:75], v[96:99], v[152:155]
	v_mfma_f32_16x16x32_bf16 v[156:159], v[76:79], v[96:99], v[156:159]
	v_mfma_f32_16x16x32_bf16 v[160:163], v[80:83], v[96:99], v[160:163]
	v_mfma_f32_16x16x32_bf16 v[164:167], v[84:87], v[96:99], v[164:167]
	s_add_u32 s42, s41, 0x4000
	buffer_load_dwordx4 v[12:15], v1, s[4:7], s42 offen sc0 nt
	v_mfma_f32_16x16x32_bf16 v[168:171], v[72:75], v[100:103], v[168:171]
	v_mfma_f32_16x16x32_bf16 v[172:175], v[76:79], v[100:103], v[172:175]
	v_mfma_f32_16x16x32_bf16 v[176:179], v[80:83], v[100:103], v[176:179]
	v_mfma_f32_16x16x32_bf16 v[180:183], v[84:87], v[100:103], v[180:183]
	v_mfma_f32_16x16x32_bf16 v[184:187], v[72:75], v[104:107], v[184:187]
	v_mfma_f32_16x16x32_bf16 v[188:191], v[76:79], v[104:107], v[188:191]
	v_mfma_f32_16x16x32_bf16 v[192:195], v[80:83], v[104:107], v[192:195]
	v_mfma_f32_16x16x32_bf16 v[196:199], v[84:87], v[104:107], v[196:199]
	s_add_u32 s42, s41, 0x8000
	buffer_load_dwordx4 v[16:19], v1, s[4:7], s42 offen sc0 nt
	v_mfma_f32_16x16x32_bf16 v[200:203], v[72:75], v[108:111], v[200:203]
	v_mfma_f32_16x16x32_bf16 v[204:207], v[76:79], v[108:111], v[204:207]
	v_mfma_f32_16x16x32_bf16 v[208:211], v[80:83], v[108:111], v[208:211]
	v_mfma_f32_16x16x32_bf16 v[212:215], v[84:87], v[108:111], v[212:215]
	v_mfma_f32_16x16x32_bf16 v[216:219], v[72:75], v[112:115], v[216:219]
	v_mfma_f32_16x16x32_bf16 v[220:223], v[76:79], v[112:115], v[220:223]
	v_mfma_f32_16x16x32_bf16 v[224:227], v[80:83], v[112:115], v[224:227]
	v_mfma_f32_16x16x32_bf16 v[228:231], v[84:87], v[112:115], v[228:231]
	s_add_u32 s42, s41, 0xc000
	buffer_load_dwordx4 v[20:23], v1, s[4:7], s42 offen sc0 nt
	v_mfma_f32_16x16x32_bf16 v[232:235], v[72:75], v[116:119], v[232:235]
	v_mfma_f32_16x16x32_bf16 v[236:239], v[76:79], v[116:119], v[236:239]
	v_mfma_f32_16x16x32_bf16 v[240:243], v[80:83], v[116:119], v[240:243]
	v_mfma_f32_16x16x32_bf16 v[244:247], v[84:87], v[116:119], v[244:247]
	s_barrier
	ds_read_b128 v[72:75], v6 offset:1024
	ds_read_b128 v[76:79], v6 offset:3072
	ds_read_b128 v[80:83], v6 offset:5120
	ds_read_b128 v[84:87], v6 offset:7168
	ds_read_b128 v[88:91], v4 offset:33792
	ds_read_b128 v[92:95], v4 offset:35840
	ds_read_b128 v[96:99], v4 offset:37888
	ds_read_b128 v[100:103], v4 offset:39936
	ds_read_b128 v[104:107], v4 offset:41984
	ds_read_b128 v[108:111], v4 offset:44032
	ds_read_b128 v[112:115], v4 offset:46080
	ds_read_b128 v[116:119], v4 offset:48128
	s_waitcnt vmcnt(56)
	v_cvt_pk_bf16_f32 v24, v24, v25
	v_cvt_pk_bf16_f32 v25, v26, v27
	v_cvt_pk_bf16_f32 v28, v28, v29
	v_cvt_pk_bf16_f32 v29, v30, v31
	ds_write2st64_b64 v3, v[24:25], v[28:29] offset0:32 offset1:40
	s_waitcnt vmcnt(52)
	v_cvt_pk_bf16_f32 v32, v32, v33
	v_cvt_pk_bf16_f32 v33, v34, v35
	v_cvt_pk_bf16_f32 v36, v36, v37
	v_cvt_pk_bf16_f32 v37, v38, v39
	ds_write2st64_b64 v3, v[32:33], v[36:37] offset0:48 offset1:56
	s_waitcnt vmcnt(44)
	s_waitcnt lgkmcnt(0)
	s_barrier
	v_mfma_f32_16x16x32_bf16 v[120:123], v[72:75], v[88:91], v[120:123]
	s_add_u32 s33, s33, 0x8000
	s_cmp_eq_u32 s33, 0x18000
	s_cselect_b32 s33, 0, s33
	s_add_u32 s25, s25, 1
	s_mov_b32 m0, s26
	v_mfma_f32_16x16x32_bf16 v[124:127], v[76:79], v[88:91], v[124:127]
	buffer_load_dwordx4 v2, s[12:15], s44 offen sc1 lds
	v_mfma_f32_16x16x32_bf16 v[128:131], v[80:83], v[88:91], v[128:131]
	v_mfma_f32_16x16x32_bf16 v[132:135], v[84:87], v[88:91], v[132:135]
	v_mfma_f32_16x16x32_bf16 v[136:139], v[72:75], v[92:95], v[136:139]
	v_mfma_f32_16x16x32_bf16 v[140:143], v[76:79], v[92:95], v[140:143]
	s_add_u32 s42, s41, 0x10000
	buffer_load_dwordx4 v[24:27], v1, s[4:7], s42 offen sc0 nt
	v_mfma_f32_16x16x32_bf16 v[144:147], v[80:83], v[92:95], v[144:147]
	v_mfma_f32_16x16x32_bf16 v[148:151], v[84:87], v[92:95], v[148:151]
	v_mfma_f32_16x16x32_bf16 v[152:155], v[72:75], v[96:99], v[152:155]
	v_mfma_f32_16x16x32_bf16 v[156:159], v[76:79], v[96:99], v[156:159]
	buffer_load_dwordx4 v2, s[12:15], s44 offen offset:1024 sc1 lds
	v_mfma_f32_16x16x32_bf16 v[160:163], v[80:83], v[96:99], v[160:163]
	v_mfma_f32_16x16x32_bf16 v[164:167], v[84:87], v[96:99], v[164:167]
	v_mfma_f32_16x16x32_bf16 v[168:171], v[72:75], v[100:103], v[168:171]
	v_mfma_f32_16x16x32_bf16 v[172:175], v[76:79], v[100:103], v[172:175]
	s_add_u32 s42, s41, 0x14000
	buffer_load_dwordx4 v[28:31], v1, s[4:7], s42 offen sc0 nt
	v_mfma_f32_16x16x32_bf16 v[176:179], v[80:83], v[100:103], v[176:179]
	v_mfma_f32_16x16x32_bf16 v[180:183], v[84:87], v[100:103], v[180:183]
	v_mfma_f32_16x16x32_bf16 v[184:187], v[72:75], v[104:107], v[184:187]
	v_mfma_f32_16x16x32_bf16 v[188:191], v[76:79], v[104:107], v[188:191]
	buffer_load_dwordx4 v2, s[12:15], s44 offen offset:2048 sc1 lds
	v_mfma_f32_16x16x32_bf16 v[192:195], v[80:83], v[104:107], v[192:195]
	v_mfma_f32_16x16x32_bf16 v[196:199], v[84:87], v[104:107], v[196:199]
	v_mfma_f32_16x16x32_bf16 v[200:203], v[72:75], v[108:111], v[200:203]
	v_mfma_f32_16x16x32_bf16 v[204:207], v[76:79], v[108:111], v[204:207]
	s_add_u32 s42, s41, 0x18000
	buffer_load_dwordx4 v[32:35], v1, s[4:7], s42 offen sc0 nt
	v_mfma_f32_16x16x32_bf16 v[208:211], v[80:83], v[108:111], v[208:211]
	v_mfma_f32_16x16x32_bf16 v[212:215], v[84:87], v[108:111], v[212:215]
	v_mfma_f32_16x16x32_bf16 v[216:219], v[72:75], v[112:115], v[216:219]
	v_mfma_f32_16x16x32_bf16 v[220:223], v[76:79], v[112:115], v[220:223]
	buffer_load_dwordx4 v2, s[12:15], s44 offen offset:3072 sc1 lds
	v_mfma_f32_16x16x32_bf16 v[224:227], v[80:83], v[112:115], v[224:227]
	v_mfma_f32_16x16x32_bf16 v[228:231], v[84:87], v[112:115], v[228:231]
	v_mfma_f32_16x16x32_bf16 v[232:235], v[72:75], v[116:119], v[232:235]
	v_mfma_f32_16x16x32_bf16 v[236:239], v[76:79], v[116:119], v[236:239]
	s_add_u32 s42, s41, 0x1c000
	buffer_load_dwordx4 v[36:39], v1, s[4:7], s42 offen sc0 nt
	v_mfma_f32_16x16x32_bf16 v[240:243], v[80:83], v[116:119], v[240:243]
	s_add_u32 s26, s26, 0x8000
	s_cmp_eq_u32 s26, s32
	s_cselect_b32 s26, s27, s26
	v_mfma_f32_16x16x32_bf16 v[244:247], v[84:87], v[116:119], v[244:247]
	s_barrier
	v_add_u32_e32 v6, s33, v5
	ds_read_b128 v[72:75], v6 offset:0
	ds_read_b128 v[76:79], v6 offset:2048
	ds_read_b128 v[80:83], v6 offset:4096
	ds_read_b128 v[84:87], v6 offset:6144
	ds_read_b128 v[88:91], v4 offset:0
	ds_read_b128 v[92:95], v4 offset:2048
	ds_read_b128 v[96:99], v4 offset:4096
	ds_read_b128 v[100:103], v4 offset:6144
	ds_read_b128 v[104:107], v4 offset:8192
	ds_read_b128 v[108:111], v4 offset:10240
	ds_read_b128 v[112:115], v4 offset:12288
	ds_read_b128 v[116:119], v4 offset:14336
	s_waitcnt vmcnt(18)
	v_cvt_pk_bf16_f32 v40, v40, v41
	v_cvt_pk_bf16_f32 v41, v42, v43
	v_cvt_pk_bf16_f32 v44, v44, v45
	v_cvt_pk_bf16_f32 v45, v46, v47
	ds_write2st64_b64 v3, v[40:41], v[44:45] offset0:64 offset1:72
	s_waitcnt vmcnt(16)
	v_cvt_pk_bf16_f32 v48, v48, v49
	v_cvt_pk_bf16_f32 v49, v50, v51
	v_cvt_pk_bf16_f32 v52, v52, v53
	v_cvt_pk_bf16_f32 v53, v54, v55
	ds_write2st64_b64 v3, v[48:49], v[52:53] offset0:80 offset1:88
	s_waitcnt lgkmcnt(0)
	s_barrier
	v_mfma_f32_16x16x32_bf16 v[120:123], v[72:75], v[88:91], v[120:123]
	s_min_u32 s40, s25, 31
	s_bitcmp1_b32 s40, 4
	s_cselect_b32 s41, s23, s22
	s_lshl_b32 s42, s40, 23
	s_and_b32 s42, s42, 0x7000000
	s_or_b32 s41, s41, s42
	s_lshl_b32 s42, s40, 8
	s_and_b32 s42, s42, 0x100
	s_or_b32 s41, s41, s42
	s_sub_u32 s43, s25, 1
	s_min_u32 s43, s43, 31
	s_and_b32 s43, s43, 15
	s_lshl_b32 s43, s43, 15
	s_add_u32 s44, s43, s24
	v_mfma_f32_16x16x32_bf16 v[124:127], v[76:79], v[88:91], v[124:127]
	v_mfma_f32_16x16x32_bf16 v[128:131], v[80:83], v[88:91], v[128:131]
	v_mfma_f32_16x16x32_bf16 v[132:135], v[84:87], v[88:91], v[132:135]
	buffer_load_dwordx4 v[40:43], v1, s[4:7], s41 offen sc0 nt
	v_mfma_f32_16x16x32_bf16 v[136:139], v[72:75], v[92:95], v[136:139]
	v_mfma_f32_16x16x32_bf16 v[140:143], v[76:79], v[92:95], v[140:143]
	v_mfma_f32_16x16x32_bf16 v[144:147], v[80:83], v[92:95], v[144:147]
	v_mfma_f32_16x16x32_bf16 v[148:151], v[84:87], v[92:95], v[148:151]
	v_mfma_f32_16x16x32_bf16 v[152:155], v[72:75], v[96:99], v[152:155]
	v_mfma_f32_16x16x32_bf16 v[156:159], v[76:79], v[96:99], v[156:159]
	v_mfma_f32_16x16x32_bf16 v[160:163], v[80:83], v[96:99], v[160:163]
	v_mfma_f32_16x16x32_bf16 v[164:167], v[84:87], v[96:99], v[164:167]
	s_add_u32 s42, s41, 0x4000
	buffer_load_dwordx4 v[44:47], v1, s[4:7], s42 offen sc0 nt
	v_mfma_f32_16x16x32_bf16 v[168:171], v[72:75], v[100:103], v[168:171]
	v_mfma_f32_16x16x32_bf16 v[172:175], v[76:79], v[100:103], v[172:175]
	v_mfma_f32_16x16x32_bf16 v[176:179], v[80:83], v[100:103], v[176:179]
	v_mfma_f32_16x16x32_bf16 v[180:183], v[84:87], v[100:103], v[180:183]
	v_mfma_f32_16x16x32_bf16 v[184:187], v[72:75], v[104:107], v[184:187]
	v_mfma_f32_16x16x32_bf16 v[188:191], v[76:79], v[104:107], v[188:191]
	v_mfma_f32_16x16x32_bf16 v[192:195], v[80:83], v[104:107], v[192:195]
	v_mfma_f32_16x16x32_bf16 v[196:199], v[84:87], v[104:107], v[196:199]
	s_add_u32 s42, s41, 0x8000
	buffer_load_dwordx4 v[48:51], v1, s[4:7], s42 offen sc0 nt
	v_mfma_f32_16x16x32_bf16 v[200:203], v[72:75], v[108:111], v[200:203]
	v_mfma_f32_16x16x32_bf16 v[204:207], v[76:79], v[108:111], v[204:207]
	v_mfma_f32_16x16x32_bf16 v[208:211], v[80:83], v[108:111], v[208:211]
	v_mfma_f32_16x16x32_bf16 v[212:215], v[84:87], v[108:111], v[212:215]
	v_mfma_f32_16x16x32_bf16 v[216:219], v[72:75], v[112:115], v[216:219]
	v_mfma_f32_16x16x32_bf16 v[220:223], v[76:79], v[112:115], v[220:223]
	v_mfma_f32_16x16x32_bf16 v[224:227], v[80:83], v[112:115], v[224:227]
	v_mfma_f32_16x16x32_bf16 v[228:231], v[84:87], v[112:115], v[228:231]
	s_add_u32 s42, s41, 0xc000
	buffer_load_dwordx4 v[52:55], v1, s[4:7], s42 offen sc0 nt
	v_mfma_f32_16x16x32_bf16 v[232:235], v[72:75], v[116:119], v[232:235]
	v_mfma_f32_16x16x32_bf16 v[236:239], v[76:79], v[116:119], v[236:239]
	v_mfma_f32_16x16x32_bf16 v[240:243], v[80:83], v[116:119], v[240:243]
	v_mfma_f32_16x16x32_bf16 v[244:247], v[84:87], v[116:119], v[244:247]
	s_barrier
	ds_read_b128 v[72:75], v6 offset:1024
	ds_read_b128 v[76:79], v6 offset:3072
	ds_read_b128 v[80:83], v6 offset:5120
	ds_read_b128 v[84:87], v6 offset:7168
	ds_read_b128 v[88:91], v4 offset:1024
	ds_read_b128 v[92:95], v4 offset:3072
	ds_read_b128 v[96:99], v4 offset:5120
	ds_read_b128 v[100:103], v4 offset:7168
	ds_read_b128 v[104:107], v4 offset:9216
	ds_read_b128 v[108:111], v4 offset:11264
	ds_read_b128 v[112:115], v4 offset:13312
	ds_read_b128 v[116:119], v4 offset:15360
	s_waitcnt vmcnt(18)
	v_cvt_pk_bf16_f32 v56, v56, v57
	v_cvt_pk_bf16_f32 v57, v58, v59
	v_cvt_pk_bf16_f32 v60, v60, v61
	v_cvt_pk_bf16_f32 v61, v62, v63
	ds_write2st64_b64 v3, v[56:57], v[60:61] offset0:96 offset1:104
	s_waitcnt vmcnt(16)
	v_cvt_pk_bf16_f32 v64, v64, v65
	v_cvt_pk_bf16_f32 v65, v66, v67
	v_cvt_pk_bf16_f32 v68, v68, v69
	v_cvt_pk_bf16_f32 v69, v70, v71
	ds_write2st64_b64 v3, v[64:65], v[68:69] offset0:112 offset1:120
	s_waitcnt vmcnt(5)
	s_waitcnt lgkmcnt(0)
	s_barrier
	v_mfma_f32_16x16x32_bf16 v[120:123], v[72:75], v[88:91], v[120:123]
	s_add_u32 s33, s33, 0x8000
	s_cmp_eq_u32 s33, 0x18000
	s_cselect_b32 s33, 0, s33
	s_add_u32 s25, s25, 1
	s_mov_b32 m0, s26
	v_mfma_f32_16x16x32_bf16 v[124:127], v[76:79], v[88:91], v[124:127]
	buffer_load_dwordx4 v2, s[12:15], s44 offen sc1 lds
	v_mfma_f32_16x16x32_bf16 v[128:131], v[80:83], v[88:91], v[128:131]
	v_mfma_f32_16x16x32_bf16 v[132:135], v[84:87], v[88:91], v[132:135]
	v_mfma_f32_16x16x32_bf16 v[136:139], v[72:75], v[92:95], v[136:139]
	v_mfma_f32_16x16x32_bf16 v[140:143], v[76:79], v[92:95], v[140:143]
	s_add_u32 s42, s41, 0x10000
	buffer_load_dwordx4 v[56:59], v1, s[4:7], s42 offen sc0 nt
	v_mfma_f32_16x16x32_bf16 v[144:147], v[80:83], v[92:95], v[144:147]
	v_mfma_f32_16x16x32_bf16 v[148:151], v[84:87], v[92:95], v[148:151]
	v_mfma_f32_16x16x32_bf16 v[152:155], v[72:75], v[96:99], v[152:155]
	v_mfma_f32_16x16x32_bf16 v[156:159], v[76:79], v[96:99], v[156:159]
	buffer_load_dwordx4 v2, s[12:15], s44 offen offset:1024 sc1 lds
	v_mfma_f32_16x16x32_bf16 v[160:163], v[80:83], v[96:99], v[160:163]
	v_mfma_f32_16x16x32_bf16 v[164:167], v[84:87], v[96:99], v[164:167]
	v_mfma_f32_16x16x32_bf16 v[168:171], v[72:75], v[100:103], v[168:171]
	v_mfma_f32_16x16x32_bf16 v[172:175], v[76:79], v[100:103], v[172:175]
	s_add_u32 s42, s41, 0x14000
	buffer_load_dwordx4 v[60:63], v1, s[4:7], s42 offen sc0 nt
	v_mfma_f32_16x16x32_bf16 v[176:179], v[80:83], v[100:103], v[176:179]
	v_mfma_f32_16x16x32_bf16 v[180:183], v[84:87], v[100:103], v[180:183]
	v_mfma_f32_16x16x32_bf16 v[184:187], v[72:75], v[104:107], v[184:187]
	v_mfma_f32_16x16x32_bf16 v[188:191], v[76:79], v[104:107], v[188:191]
	buffer_load_dwordx4 v2, s[12:15], s44 offen offset:2048 sc1 lds
	v_mfma_f32_16x16x32_bf16 v[192:195], v[80:83], v[104:107], v[192:195]
	v_mfma_f32_16x16x32_bf16 v[196:199], v[84:87], v[104:107], v[196:199]
	v_mfma_f32_16x16x32_bf16 v[200:203], v[72:75], v[108:111], v[200:203]
	v_mfma_f32_16x16x32_bf16 v[204:207], v[76:79], v[108:111], v[204:207]
	s_add_u32 s42, s41, 0x18000
	buffer_load_dwordx4 v[64:67], v1, s[4:7], s42 offen sc0 nt
	v_mfma_f32_16x16x32_bf16 v[208:211], v[80:83], v[108:111], v[208:211]
	v_mfma_f32_16x16x32_bf16 v[212:215], v[84:87], v[108:111], v[212:215]
	v_mfma_f32_16x16x32_bf16 v[216:219], v[72:75], v[112:115], v[216:219]
	v_mfma_f32_16x16x32_bf16 v[220:223], v[76:79], v[112:115], v[220:223]
	buffer_load_dwordx4 v2, s[12:15], s44 offen offset:3072 sc1 lds
	v_mfma_f32_16x16x32_bf16 v[224:227], v[80:83], v[112:115], v[224:227]
	v_mfma_f32_16x16x32_bf16 v[228:231], v[84:87], v[112:115], v[228:231]
	v_mfma_f32_16x16x32_bf16 v[232:235], v[72:75], v[116:119], v[232:235]
	v_mfma_f32_16x16x32_bf16 v[236:239], v[76:79], v[116:119], v[236:239]
	s_add_u32 s42, s41, 0x1c000
	buffer_load_dwordx4 v[68:71], v1, s[4:7], s42 offen sc0 nt
	v_mfma_f32_16x16x32_bf16 v[240:243], v[80:83], v[116:119], v[240:243]
	s_add_u32 s26, s26, 0x8000
	s_cmp_eq_u32 s26, s32
	s_cselect_b32 s26, s27, s26
	v_mfma_f32_16x16x32_bf16 v[244:247], v[84:87], v[116:119], v[244:247]
	s_barrier
	v_add_u32_e32 v6, s33, v5
	ds_read_b128 v[72:75], v6 offset:0
	ds_read_b128 v[76:79], v6 offset:2048
	ds_read_b128 v[80:83], v6 offset:4096
	ds_read_b128 v[84:87], v6 offset:6144
	ds_read_b128 v[88:91], v4 offset:32768
	ds_read_b128 v[92:95], v4 offset:34816
	ds_read_b128 v[96:99], v4 offset:36864
	ds_read_b128 v[100:103], v4 offset:38912
	ds_read_b128 v[104:107], v4 offset:40960
	ds_read_b128 v[108:111], v4 offset:43008
	ds_read_b128 v[112:115], v4 offset:45056
	ds_read_b128 v[116:119], v4 offset:47104
	s_waitcnt vmcnt(22)
	v_cvt_pk_bf16_f32 v8, v8, v9
	v_cvt_pk_bf16_f32 v9, v10, v11
	v_cvt_pk_bf16_f32 v12, v12, v13
	v_cvt_pk_bf16_f32 v13, v14, v15
	ds_write2st64_b64 v3, v[8:9], v[12:13] offset0:0 offset1:8
	s_waitcnt vmcnt(20)
	v_cvt_pk_bf16_f32 v16, v16, v17
	v_cvt_pk_bf16_f32 v17, v18, v19
	v_cvt_pk_bf16_f32 v20, v20, v21
	v_cvt_pk_bf16_f32 v21, v22, v23
	ds_write2st64_b64 v3, v[16:17], v[20:21] offset0:16 offset1:24
	s_waitcnt lgkmcnt(0)
	s_barrier
	v_mfma_f32_16x16x32_bf16 v[120:123], v[72:75], v[88:91], v[120:123]
	s_min_u32 s40, s25, 31
	s_bitcmp1_b32 s40, 4
	s_cselect_b32 s41, s23, s22
	s_lshl_b32 s42, s40, 23
	s_and_b32 s42, s42, 0x7000000
	s_or_b32 s41, s41, s42
	s_lshl_b32 s42, s40, 8
	s_and_b32 s42, s42, 0x100
	s_or_b32 s41, s41, s42
	s_sub_u32 s43, s25, 1
	s_min_u32 s43, s43, 31
	s_and_b32 s43, s43, 15
	s_lshl_b32 s43, s43, 15
	s_add_u32 s44, s43, s24
	v_mfma_f32_16x16x32_bf16 v[124:127], v[76:79], v[88:91], v[124:127]
	v_mfma_f32_16x16x32_bf16 v[128:131], v[80:83], v[88:91], v[128:131]
	v_mfma_f32_16x16x32_bf16 v[132:135], v[84:87], v[88:91], v[132:135]
	buffer_load_dwordx4 v[8:11], v1, s[4:7], s41 offen sc0 nt
	v_mfma_f32_16x16x32_bf16 v[136:139], v[72:75], v[92:95], v[136:139]
	v_mfma_f32_16x16x32_bf16 v[140:143], v[76:79], v[92:95], v[140:143]
	v_mfma_f32_16x16x32_bf16 v[144:147], v[80:83], v[92:95], v[144:147]
	v_mfma_f32_16x16x32_bf16 v[148:151], v[84:87], v[92:95], v[148:151]
	v_mfma_f32_16x16x32_bf16 v[152:155], v[72:75], v[96:99], v[152:155]
	v_mfma_f32_16x16x32_bf16 v[156:159], v[76:79], v[96:99], v[156:159]
	v_mfma_f32_16x16x32_bf16 v[160:163], v[80:83], v[96:99], v[160:163]
	v_mfma_f32_16x16x32_bf16 v[164:167], v[84:87], v[96:99], v[164:167]
	s_add_u32 s42, s41, 0x4000
	buffer_load_dwordx4 v[12:15], v1, s[4:7], s42 offen sc0 nt
	v_mfma_f32_16x16x32_bf16 v[168:171], v[72:75], v[100:103], v[168:171]
	v_mfma_f32_16x16x32_bf16 v[172:175], v[76:79], v[100:103], v[172:175]
	v_mfma_f32_16x16x32_bf16 v[176:179], v[80:83], v[100:103], v[176:179]
	v_mfma_f32_16x16x32_bf16 v[180:183], v[84:87], v[100:103], v[180:183]
	v_mfma_f32_16x16x32_bf16 v[184:187], v[72:75], v[104:107], v[184:187]
	v_mfma_f32_16x16x32_bf16 v[188:191], v[76:79], v[104:107], v[188:191]
	v_mfma_f32_16x16x32_bf16 v[192:195], v[80:83], v[104:107], v[192:195]
	v_mfma_f32_16x16x32_bf16 v[196:199], v[84:87], v[104:107], v[196:199]
	s_add_u32 s42, s41, 0x8000
	buffer_load_dwordx4 v[16:19], v1, s[4:7], s42 offen sc0 nt
	v_mfma_f32_16x16x32_bf16 v[200:203], v[72:75], v[108:111], v[200:203]
	v_mfma_f32_16x16x32_bf16 v[204:207], v[76:79], v[108:111], v[204:207]
	v_mfma_f32_16x16x32_bf16 v[208:211], v[80:83], v[108:111], v[208:211]
	v_mfma_f32_16x16x32_bf16 v[212:215], v[84:87], v[108:111], v[212:215]
	v_mfma_f32_16x16x32_bf16 v[216:219], v[72:75], v[112:115], v[216:219]
	v_mfma_f32_16x16x32_bf16 v[220:223], v[76:79], v[112:115], v[220:223]
	v_mfma_f32_16x16x32_bf16 v[224:227], v[80:83], v[112:115], v[224:227]
	v_mfma_f32_16x16x32_bf16 v[228:231], v[84:87], v[112:115], v[228:231]
	s_add_u32 s42, s41, 0xc000
	buffer_load_dwordx4 v[20:23], v1, s[4:7], s42 offen sc0 nt
	v_mfma_f32_16x16x32_bf16 v[232:235], v[72:75], v[116:119], v[232:235]
	v_mfma_f32_16x16x32_bf16 v[236:239], v[76:79], v[116:119], v[236:239]
	v_mfma_f32_16x16x32_bf16 v[240:243], v[80:83], v[116:119], v[240:243]
	v_mfma_f32_16x16x32_bf16 v[244:247], v[84:87], v[116:119], v[244:247]
	s_barrier
	ds_read_b128 v[72:75], v6 offset:1024
	ds_read_b128 v[76:79], v6 offset:3072
	ds_read_b128 v[80:83], v6 offset:5120
	ds_read_b128 v[84:87], v6 offset:7168
	ds_read_b128 v[88:91], v4 offset:33792
	ds_read_b128 v[92:95], v4 offset:35840
	ds_read_b128 v[96:99], v4 offset:37888
	ds_read_b128 v[100:103], v4 offset:39936
	ds_read_b128 v[104:107], v4 offset:41984
	ds_read_b128 v[108:111], v4 offset:44032
	ds_read_b128 v[112:115], v4 offset:46080
	ds_read_b128 v[116:119], v4 offset:48128
	s_waitcnt vmcnt(20)
	v_cvt_pk_bf16_f32 v24, v24, v25
	v_cvt_pk_bf16_f32 v25, v26, v27
	v_cvt_pk_bf16_f32 v28, v28, v29
	v_cvt_pk_bf16_f32 v29, v30, v31
	ds_write2st64_b64 v3, v[24:25], v[28:29] offset0:32 offset1:40
	s_waitcnt vmcnt(16)
	v_cvt_pk_bf16_f32 v32, v32, v33
	v_cvt_pk_bf16_f32 v33, v34, v35
	v_cvt_pk_bf16_f32 v36, v36, v37
	v_cvt_pk_bf16_f32 v37, v38, v39
	ds_write2st64_b64 v3, v[32:33], v[36:37] offset0:48 offset1:56
	s_waitcnt vmcnt(5)
	s_waitcnt lgkmcnt(0)
	s_barrier
	v_mfma_f32_16x16x32_bf16 v[120:123], v[72:75], v[88:91], v[120:123]
	s_add_u32 s33, s33, 0x8000
	s_cmp_eq_u32 s33, 0x18000
	s_cselect_b32 s33, 0, s33
	s_add_u32 s25, s25, 1
	s_mov_b32 m0, s26
	v_mfma_f32_16x16x32_bf16 v[124:127], v[76:79], v[88:91], v[124:127]
	buffer_load_dwordx4 v2, s[12:15], s44 offen sc1 lds
	v_mfma_f32_16x16x32_bf16 v[128:131], v[80:83], v[88:91], v[128:131]
	v_mfma_f32_16x16x32_bf16 v[132:135], v[84:87], v[88:91], v[132:135]
	v_mfma_f32_16x16x32_bf16 v[136:139], v[72:75], v[92:95], v[136:139]
	v_mfma_f32_16x16x32_bf16 v[140:143], v[76:79], v[92:95], v[140:143]
	s_add_u32 s42, s41, 0x10000
	buffer_load_dwordx4 v[24:27], v1, s[4:7], s42 offen sc0 nt
	v_mfma_f32_16x16x32_bf16 v[144:147], v[80:83], v[92:95], v[144:147]
	v_mfma_f32_16x16x32_bf16 v[148:151], v[84:87], v[92:95], v[148:151]
	v_mfma_f32_16x16x32_bf16 v[152:155], v[72:75], v[96:99], v[152:155]
	v_mfma_f32_16x16x32_bf16 v[156:159], v[76:79], v[96:99], v[156:159]
	buffer_load_dwordx4 v2, s[12:15], s44 offen offset:1024 sc1 lds
	v_mfma_f32_16x16x32_bf16 v[160:163], v[80:83], v[96:99], v[160:163]
	v_mfma_f32_16x16x32_bf16 v[164:167], v[84:87], v[96:99], v[164:167]
	v_mfma_f32_16x16x32_bf16 v[168:171], v[72:75], v[100:103], v[168:171]
	v_mfma_f32_16x16x32_bf16 v[172:175], v[76:79], v[100:103], v[172:175]
	s_add_u32 s42, s41, 0x14000
	buffer_load_dwordx4 v[28:31], v1, s[4:7], s42 offen sc0 nt
	v_mfma_f32_16x16x32_bf16 v[176:179], v[80:83], v[100:103], v[176:179]
	v_mfma_f32_16x16x32_bf16 v[180:183], v[84:87], v[100:103], v[180:183]
	v_mfma_f32_16x16x32_bf16 v[184:187], v[72:75], v[104:107], v[184:187]
	v_mfma_f32_16x16x32_bf16 v[188:191], v[76:79], v[104:107], v[188:191]
	buffer_load_dwordx4 v2, s[12:15], s44 offen offset:2048 sc1 lds
	v_mfma_f32_16x16x32_bf16 v[192:195], v[80:83], v[104:107], v[192:195]
	v_mfma_f32_16x16x32_bf16 v[196:199], v[84:87], v[104:107], v[196:199]
	v_mfma_f32_16x16x32_bf16 v[200:203], v[72:75], v[108:111], v[200:203]
	v_mfma_f32_16x16x32_bf16 v[204:207], v[76:79], v[108:111], v[204:207]
	s_add_u32 s42, s41, 0x18000
	buffer_load_dwordx4 v[32:35], v1, s[4:7], s42 offen sc0 nt
	v_mfma_f32_16x16x32_bf16 v[208:211], v[80:83], v[108:111], v[208:211]
	v_mfma_f32_16x16x32_bf16 v[212:215], v[84:87], v[108:111], v[212:215]
	v_mfma_f32_16x16x32_bf16 v[216:219], v[72:75], v[112:115], v[216:219]
	v_mfma_f32_16x16x32_bf16 v[220:223], v[76:79], v[112:115], v[220:223]
	buffer_load_dwordx4 v2, s[12:15], s44 offen offset:3072 sc1 lds
	v_mfma_f32_16x16x32_bf16 v[224:227], v[80:83], v[112:115], v[224:227]
	v_mfma_f32_16x16x32_bf16 v[228:231], v[84:87], v[112:115], v[228:231]
	v_mfma_f32_16x16x32_bf16 v[232:235], v[72:75], v[116:119], v[232:235]
	v_mfma_f32_16x16x32_bf16 v[236:239], v[76:79], v[116:119], v[236:239]
	s_add_u32 s42, s41, 0x1c000
	buffer_load_dwordx4 v[36:39], v1, s[4:7], s42 offen sc0 nt
	v_mfma_f32_16x16x32_bf16 v[240:243], v[80:83], v[116:119], v[240:243]
	s_add_u32 s26, s26, 0x8000
	s_cmp_eq_u32 s26, s32
	s_cselect_b32 s26, s27, s26
	v_mfma_f32_16x16x32_bf16 v[244:247], v[84:87], v[116:119], v[244:247]
	s_barrier
	s_mov_b32 s38, 4
.Lg_loop1:
	v_add_u32_e32 v6, s33, v5
	ds_read_b128 v[72:75], v6 offset:0
	ds_read_b128 v[76:79], v6 offset:2048
	ds_read_b128 v[80:83], v6 offset:4096
	ds_read_b128 v[84:87], v6 offset:6144
	ds_read_b128 v[88:91], v4 offset:0
	ds_read_b128 v[92:95], v4 offset:2048
	ds_read_b128 v[96:99], v4 offset:4096
	ds_read_b128 v[100:103], v4 offset:6144
	ds_read_b128 v[104:107], v4 offset:8192
	ds_read_b128 v[108:111], v4 offset:10240
	ds_read_b128 v[112:115], v4 offset:12288
	ds_read_b128 v[116:119], v4 offset:14336
	s_waitcnt vmcnt(22)
	v_cvt_pk_bf16_f32 v40, v40, v41
	v_cvt_pk_bf16_f32 v41, v42, v43
	v_cvt_pk_bf16_f32 v44, v44, v45
	v_cvt_pk_bf16_f32 v45, v46, v47
	ds_write2st64_b64 v3, v[40:41], v[44:45] offset0:64 offset1:72
	s_waitcnt vmcnt(20)
	v_cvt_pk_bf16_f32 v48, v48, v49
	v_cvt_pk_bf16_f32 v49, v50, v51
	v_cvt_pk_bf16_f32 v52, v52, v53
	v_cvt_pk_bf16_f32 v53, v54, v55
	ds_write2st64_b64 v3, v[48:49], v[52:53] offset0:80 offset1:88
	s_waitcnt lgkmcnt(0)
	s_barrier
	v_mfma_f32_16x16x32_bf16 v[120:123], v[72:75], v[88:91], v[120:123]
	s_min_u32 s40, s25, 31
	s_bitcmp1_b32 s40, 4
	s_cselect_b32 s41, s23, s22
	s_lshl_b32 s42, s40, 23
	s_and_b32 s42, s42, 0x7000000
	s_or_b32 s41, s41, s42
	s_lshl_b32 s42, s40, 8
	s_and_b32 s42, s42, 0x100
	s_or_b32 s41, s41, s42
	s_sub_u32 s43, s25, 1
	s_min_u32 s43, s43, 31
	s_and_b32 s43, s43, 15
	s_lshl_b32 s43, s43, 15
	s_add_u32 s44, s43, s24
	v_mfma_f32_16x16x32_bf16 v[124:127], v[76:79], v[88:91], v[124:127]
	v_mfma_f32_16x16x32_bf16 v[128:131], v[80:83], v[88:91], v[128:131]
	v_mfma_f32_16x16x32_bf16 v[132:135], v[84:87], v[88:91], v[132:135]
	buffer_load_dwordx4 v[40:43], v1, s[4:7], s41 offen sc0 nt
	v_mfma_f32_16x16x32_bf16 v[136:139], v[72:75], v[92:95], v[136:139]
	v_mfma_f32_16x16x32_bf16 v[140:143], v[76:79], v[92:95], v[140:143]
	v_mfma_f32_16x16x32_bf16 v[144:147], v[80:83], v[92:95], v[144:147]
	v_mfma_f32_16x16x32_bf16 v[148:151], v[84:87], v[92:95], v[148:151]
	v_mfma_f32_16x16x32_bf16 v[152:155], v[72:75], v[96:99], v[152:155]
	v_mfma_f32_16x16x32_bf16 v[156:159], v[76:79], v[96:99], v[156:159]
	v_mfma_f32_16x16x32_bf16 v[160:163], v[80:83], v[96:99], v[160:163]
	v_mfma_f32_16x16x32_bf16 v[164:167], v[84:87], v[96:99], v[164:167]
	s_add_u32 s42, s41, 0x4000
	buffer_load_dwordx4 v[44:47], v1, s[4:7], s42 offen sc0 nt
	v_mfma_f32_16x16x32_bf16 v[168:171], v[72:75], v[100:103], v[168:171]
	v_mfma_f32_16x16x32_bf16 v[172:175], v[76:79], v[100:103], v[172:175]
	v_mfma_f32_16x16x32_bf16 v[176:179], v[80:83], v[100:103], v[176:179]
	v_mfma_f32_16x16x32_bf16 v[180:183], v[84:87], v[100:103], v[180:183]
	v_mfma_f32_16x16x32_bf16 v[184:187], v[72:75], v[104:107], v[184:187]
	v_mfma_f32_16x16x32_bf16 v[188:191], v[76:79], v[104:107], v[188:191]
	v_mfma_f32_16x16x32_bf16 v[192:195], v[80:83], v[104:107], v[192:195]
	v_mfma_f32_16x16x32_bf16 v[196:199], v[84:87], v[104:107], v[196:199]
	s_add_u32 s42, s41, 0x8000
	buffer_load_dwordx4 v[48:51], v1, s[4:7], s42 offen sc0 nt
	v_mfma_f32_16x16x32_bf16 v[200:203], v[72:75], v[108:111], v[200:203]
	v_mfma_f32_16x16x32_bf16 v[204:207], v[76:79], v[108:111], v[204:207]
	v_mfma_f32_16x16x32_bf16 v[208:211], v[80:83], v[108:111], v[208:211]
	v_mfma_f32_16x16x32_bf16 v[212:215], v[84:87], v[108:111], v[212:215]
	v_mfma_f32_16x16x32_bf16 v[216:219], v[72:75], v[112:115], v[216:219]
	v_mfma_f32_16x16x32_bf16 v[220:223], v[76:79], v[112:115], v[220:223]
	v_mfma_f32_16x16x32_bf16 v[224:227], v[80:83], v[112:115], v[224:227]
	v_mfma_f32_16x16x32_bf16 v[228:231], v[84:87], v[112:115], v[228:231]
	s_add_u32 s42, s41, 0xc000
	buffer_load_dwordx4 v[52:55], v1, s[4:7], s42 offen sc0 nt
	v_mfma_f32_16x16x32_bf16 v[232:235], v[72:75], v[116:119], v[232:235]
	v_mfma_f32_16x16x32_bf16 v[236:239], v[76:79], v[116:119], v[236:239]
	v_mfma_f32_16x16x32_bf16 v[240:243], v[80:83], v[116:119], v[240:243]
	v_mfma_f32_16x16x32_bf16 v[244:247], v[84:87], v[116:119], v[244:247]
	s_barrier
	ds_read_b128 v[72:75], v6 offset:1024
	ds_read_b128 v[76:79], v6 offset:3072
	ds_read_b128 v[80:83], v6 offset:5120
	ds_read_b128 v[84:87], v6 offset:7168
	ds_read_b128 v[88:91], v4 offset:1024
	ds_read_b128 v[92:95], v4 offset:3072
	ds_read_b128 v[96:99], v4 offset:5120
	ds_read_b128 v[100:103], v4 offset:7168
	ds_read_b128 v[104:107], v4 offset:9216
	ds_read_b128 v[108:111], v4 offset:11264
	ds_read_b128 v[112:115], v4 offset:13312
	ds_read_b128 v[116:119], v4 offset:15360
	s_waitcnt vmcnt(20)
	v_cvt_pk_bf16_f32 v56, v56, v57
	v_cvt_pk_bf16_f32 v57, v58, v59
	v_cvt_pk_bf16_f32 v60, v60, v61
	v_cvt_pk_bf16_f32 v61, v62, v63
	ds_write2st64_b64 v3, v[56:57], v[60:61] offset0:96 offset1:104
	s_waitcnt vmcnt(16)
	v_cvt_pk_bf16_f32 v64, v64, v65
	v_cvt_pk_bf16_f32 v65, v66, v67
	v_cvt_pk_bf16_f32 v68, v68, v69
	v_cvt_pk_bf16_f32 v69, v70, v71
	ds_write2st64_b64 v3, v[64:65], v[68:69] offset0:112 offset1:120
	s_waitcnt vmcnt(5)
	s_waitcnt lgkmcnt(0)
	s_barrier
	v_mfma_f32_16x16x32_bf16 v[120:123], v[72:75], v[88:91], v[120:123]
	s_add_u32 s33, s33, 0x8000
	s_cmp_eq_u32 s33, 0x18000
	s_cselect_b32 s33, 0, s33
	s_add_u32 s25, s25, 1
	s_mov_b32 m0, s26
	v_mfma_f32_16x16x32_bf16 v[124:127], v[76:79], v[88:91], v[124:127]
	buffer_load_dwordx4 v2, s[12:15], s44 offen sc1 lds
	v_mfma_f32_16x16x32_bf16 v[128:131], v[80:83], v[88:91], v[128:131]
	v_mfma_f32_16x16x32_bf16 v[132:135], v[84:87], v[88:91], v[132:135]
	v_mfma_f32_16x16x32_bf16 v[136:139], v[72:75], v[92:95], v[136:139]
	v_mfma_f32_16x16x32_bf16 v[140:143], v[76:79], v[92:95], v[140:143]
	s_add_u32 s42, s41, 0x10000
	buffer_load_dwordx4 v[56:59], v1, s[4:7], s42 offen sc0 nt
	v_mfma_f32_16x16x32_bf16 v[144:147], v[80:83], v[92:95], v[144:147]
	v_mfma_f32_16x16x32_bf16 v[148:151], v[84:87], v[92:95], v[148:151]
	v_mfma_f32_16x16x32_bf16 v[152:155], v[72:75], v[96:99], v[152:155]
	v_mfma_f32_16x16x32_bf16 v[156:159], v[76:79], v[96:99], v[156:159]
	buffer_load_dwordx4 v2, s[12:15], s44 offen offset:1024 sc1 lds
	v_mfma_f32_16x16x32_bf16 v[160:163], v[80:83], v[96:99], v[160:163]
	v_mfma_f32_16x16x32_bf16 v[164:167], v[84:87], v[96:99], v[164:167]
	v_mfma_f32_16x16x32_bf16 v[168:171], v[72:75], v[100:103], v[168:171]
	v_mfma_f32_16x16x32_bf16 v[172:175], v[76:79], v[100:103], v[172:175]
	s_add_u32 s42, s41, 0x14000
	buffer_load_dwordx4 v[60:63], v1, s[4:7], s42 offen sc0 nt
	v_mfma_f32_16x16x32_bf16 v[176:179], v[80:83], v[100:103], v[176:179]
	v_mfma_f32_16x16x32_bf16 v[180:183], v[84:87], v[100:103], v[180:183]
	v_mfma_f32_16x16x32_bf16 v[184:187], v[72:75], v[104:107], v[184:187]
	v_mfma_f32_16x16x32_bf16 v[188:191], v[76:79], v[104:107], v[188:191]
	buffer_load_dwordx4 v2, s[12:15], s44 offen offset:2048 sc1 lds
	v_mfma_f32_16x16x32_bf16 v[192:195], v[80:83], v[104:107], v[192:195]
	v_mfma_f32_16x16x32_bf16 v[196:199], v[84:87], v[104:107], v[196:199]
	v_mfma_f32_16x16x32_bf16 v[200:203], v[72:75], v[108:111], v[200:203]
	v_mfma_f32_16x16x32_bf16 v[204:207], v[76:79], v[108:111], v[204:207]
	s_add_u32 s42, s41, 0x18000
	buffer_load_dwordx4 v[64:67], v1, s[4:7], s42 offen sc0 nt
	v_mfma_f32_16x16x32_bf16 v[208:211], v[80:83], v[108:111], v[208:211]
	v_mfma_f32_16x16x32_bf16 v[212:215], v[84:87], v[108:111], v[212:215]
	v_mfma_f32_16x16x32_bf16 v[216:219], v[72:75], v[112:115], v[216:219]
	v_mfma_f32_16x16x32_bf16 v[220:223], v[76:79], v[112:115], v[220:223]
	buffer_load_dwordx4 v2, s[12:15], s44 offen offset:3072 sc1 lds
	v_mfma_f32_16x16x32_bf16 v[224:227], v[80:83], v[112:115], v[224:227]
	v_mfma_f32_16x16x32_bf16 v[228:231], v[84:87], v[112:115], v[228:231]
	v_mfma_f32_16x16x32_bf16 v[232:235], v[72:75], v[116:119], v[232:235]
	v_mfma_f32_16x16x32_bf16 v[236:239], v[76:79], v[116:119], v[236:239]
	s_add_u32 s42, s41, 0x1c000
	buffer_load_dwordx4 v[68:71], v1, s[4:7], s42 offen sc0 nt
	v_mfma_f32_16x16x32_bf16 v[240:243], v[80:83], v[116:119], v[240:243]
	s_add_u32 s26, s26, 0x8000
	s_cmp_eq_u32 s26, s32
	s_cselect_b32 s26, s27, s26
	v_mfma_f32_16x16x32_bf16 v[244:247], v[84:87], v[116:119], v[244:247]
	s_barrier
	v_add_u32_e32 v6, s33, v5
	ds_read_b128 v[72:75], v6 offset:0
	ds_read_b128 v[76:79], v6 offset:2048
	ds_read_b128 v[80:83], v6 offset:4096
	ds_read_b128 v[84:87], v6 offset:6144
	ds_read_b128 v[88:91], v4 offset:32768
	ds_read_b128 v[92:95], v4 offset:34816
	ds_read_b128 v[96:99], v4 offset:36864
	ds_read_b128 v[100:103], v4 offset:38912
	ds_read_b128 v[104:107], v4 offset:40960
	ds_read_b128 v[108:111], v4 offset:43008
	ds_read_b128 v[112:115], v4 offset:45056
	ds_read_b128 v[116:119], v4 offset:47104
	s_waitcnt vmcnt(22)
	v_cvt_pk_bf16_f32 v8, v8, v9
	v_cvt_pk_bf16_f32 v9, v10, v11
	v_cvt_pk_bf16_f32 v12, v12, v13
	v_cvt_pk_bf16_f32 v13, v14, v15
	ds_write2st64_b64 v3, v[8:9], v[12:13] offset0:0 offset1:8
	s_waitcnt vmcnt(20)
	v_cvt_pk_bf16_f32 v16, v16, v17
	v_cvt_pk_bf16_f32 v17, v18, v19
	v_cvt_pk_bf16_f32 v20, v20, v21
	v_cvt_pk_bf16_f32 v21, v22, v23
	ds_write2st64_b64 v3, v[16:17], v[20:21] offset0:16 offset1:24
	s_waitcnt lgkmcnt(0)
	s_barrier
	v_mfma_f32_16x16x32_bf16 v[120:123], v[72:75], v[88:91], v[120:123]
	s_min_u32 s40, s25, 31
	s_bitcmp1_b32 s40, 4
	s_cselect_b32 s41, s23, s22
	s_lshl_b32 s42, s40, 23
	s_and_b32 s42, s42, 0x7000000
	s_or_b32 s41, s41, s42
	s_lshl_b32 s42, s40, 8
	s_and_b32 s42, s42, 0x100
	s_or_b32 s41, s41, s42
	s_sub_u32 s43, s25, 1
	s_min_u32 s43, s43, 31
	s_and_b32 s43, s43, 15
	s_lshl_b32 s43, s43, 15
	s_add_u32 s44, s43, s24
	v_mfma_f32_16x16x32_bf16 v[124:127], v[76:79], v[88:91], v[124:127]
	v_mfma_f32_16x16x32_bf16 v[128:131], v[80:83], v[88:91], v[128:131]
	v_mfma_f32_16x16x32_bf16 v[132:135], v[84:87], v[88:91], v[132:135]
	buffer_load_dwordx4 v[8:11], v1, s[4:7], s41 offen sc0 nt
	v_mfma_f32_16x16x32_bf16 v[136:139], v[72:75], v[92:95], v[136:139]
	v_mfma_f32_16x16x32_bf16 v[140:143], v[76:79], v[92:95], v[140:143]
	v_mfma_f32_16x16x32_bf16 v[144:147], v[80:83], v[92:95], v[144:147]
	v_mfma_f32_16x16x32_bf16 v[148:151], v[84:87], v[92:95], v[148:151]
	v_mfma_f32_16x16x32_bf16 v[152:155], v[72:75], v[96:99], v[152:155]
	v_mfma_f32_16x16x32_bf16 v[156:159], v[76:79], v[96:99], v[156:159]
	v_mfma_f32_16x16x32_bf16 v[160:163], v[80:83], v[96:99], v[160:163]
	v_mfma_f32_16x16x32_bf16 v[164:167], v[84:87], v[96:99], v[164:167]
	s_add_u32 s42, s41, 0x4000
	buffer_load_dwordx4 v[12:15], v1, s[4:7], s42 offen sc0 nt
	v_mfma_f32_16x16x32_bf16 v[168:171], v[72:75], v[100:103], v[168:171]
	v_mfma_f32_16x16x32_bf16 v[172:175], v[76:79], v[100:103], v[172:175]
	v_mfma_f32_16x16x32_bf16 v[176:179], v[80:83], v[100:103], v[176:179]
	v_mfma_f32_16x16x32_bf16 v[180:183], v[84:87], v[100:103], v[180:183]
	v_mfma_f32_16x16x32_bf16 v[184:187], v[72:75], v[104:107], v[184:187]
	v_mfma_f32_16x16x32_bf16 v[188:191], v[76:79], v[104:107], v[188:191]
	v_mfma_f32_16x16x32_bf16 v[192:195], v[80:83], v[104:107], v[192:195]
	v_mfma_f32_16x16x32_bf16 v[196:199], v[84:87], v[104:107], v[196:199]
	s_add_u32 s42, s41, 0x8000
	buffer_load_dwordx4 v[16:19], v1, s[4:7], s42 offen sc0 nt
	v_mfma_f32_16x16x32_bf16 v[200:203], v[72:75], v[108:111], v[200:203]
	v_mfma_f32_16x16x32_bf16 v[204:207], v[76:79], v[108:111], v[204:207]
	v_mfma_f32_16x16x32_bf16 v[208:211], v[80:83], v[108:111], v[208:211]
	v_mfma_f32_16x16x32_bf16 v[212:215], v[84:87], v[108:111], v[212:215]
	v_mfma_f32_16x16x32_bf16 v[216:219], v[72:75], v[112:115], v[216:219]
	v_mfma_f32_16x16x32_bf16 v[220:223], v[76:79], v[112:115], v[220:223]
	v_mfma_f32_16x16x32_bf16 v[224:227], v[80:83], v[112:115], v[224:227]
	v_mfma_f32_16x16x32_bf16 v[228:231], v[84:87], v[112:115], v[228:231]
	s_add_u32 s42, s41, 0xc000
	buffer_load_dwordx4 v[20:23], v1, s[4:7], s42 offen sc0 nt
	v_mfma_f32_16x16x32_bf16 v[232:235], v[72:75], v[116:119], v[232:235]
	v_mfma_f32_16x16x32_bf16 v[236:239], v[76:79], v[116:119], v[236:239]
	v_mfma_f32_16x16x32_bf16 v[240:243], v[80:83], v[116:119], v[240:243]
	v_mfma_f32_16x16x32_bf16 v[244:247], v[84:87], v[116:119], v[244:247]
	s_barrier
	ds_read_b128 v[72:75], v6 offset:1024
	ds_read_b128 v[76:79], v6 offset:3072
	ds_read_b128 v[80:83], v6 offset:5120
	ds_read_b128 v[84:87], v6 offset:7168
	ds_read_b128 v[88:91], v4 offset:33792
	ds_read_b128 v[92:95], v4 offset:35840
	ds_read_b128 v[96:99], v4 offset:37888
	ds_read_b128 v[100:103], v4 offset:39936
	ds_read_b128 v[104:107], v4 offset:41984
	ds_read_b128 v[108:111], v4 offset:44032
	ds_read_b128 v[112:115], v4 offset:46080
	ds_read_b128 v[116:119], v4 offset:48128
	s_waitcnt vmcnt(20)
	v_cvt_pk_bf16_f32 v24, v24, v25
	v_cvt_pk_bf16_f32 v25, v26, v27
	v_cvt_pk_bf16_f32 v28, v28, v29
	v_cvt_pk_bf16_f32 v29, v30, v31
	ds_write2st64_b64 v3, v[24:25], v[28:29] offset0:32 offset1:40
	s_waitcnt vmcnt(16)
	v_cvt_pk_bf16_f32 v32, v32, v33
	v_cvt_pk_bf16_f32 v33, v34, v35
	v_cvt_pk_bf16_f32 v36, v36, v37
	v_cvt_pk_bf16_f32 v37, v38, v39
	ds_write2st64_b64 v3, v[32:33], v[36:37] offset0:48 offset1:56
	s_waitcnt vmcnt(5)
	s_waitcnt lgkmcnt(0)
	s_barrier
	v_mfma_f32_16x16x32_bf16 v[120:123], v[72:75], v[88:91], v[120:123]
	s_add_u32 s33, s33, 0x8000
	s_cmp_eq_u32 s33, 0x18000
	s_cselect_b32 s33, 0, s33
	s_add_u32 s25, s25, 1
	s_mov_b32 m0, s26
	v_mfma_f32_16x16x32_bf16 v[124:127], v[76:79], v[88:91], v[124:127]
	buffer_load_dwordx4 v2, s[12:15], s44 offen sc1 lds
	v_mfma_f32_16x16x32_bf16 v[128:131], v[80:83], v[88:91], v[128:131]
	v_mfma_f32_16x16x32_bf16 v[132:135], v[84:87], v[88:91], v[132:135]
	v_mfma_f32_16x16x32_bf16 v[136:139], v[72:75], v[92:95], v[136:139]
	v_mfma_f32_16x16x32_bf16 v[140:143], v[76:79], v[92:95], v[140:143]
	s_add_u32 s42, s41, 0x10000
	buffer_load_dwordx4 v[24:27], v1, s[4:7], s42 offen sc0 nt
	v_mfma_f32_16x16x32_bf16 v[144:147], v[80:83], v[92:95], v[144:147]
	v_mfma_f32_16x16x32_bf16 v[148:151], v[84:87], v[92:95], v[148:151]
	v_mfma_f32_16x16x32_bf16 v[152:155], v[72:75], v[96:99], v[152:155]
	v_mfma_f32_16x16x32_bf16 v[156:159], v[76:79], v[96:99], v[156:159]
	buffer_load_dwordx4 v2, s[12:15], s44 offen offset:1024 sc1 lds
	v_mfma_f32_16x16x32_bf16 v[160:163], v[80:83], v[96:99], v[160:163]
	v_mfma_f32_16x16x32_bf16 v[164:167], v[84:87], v[96:99], v[164:167]
	v_mfma_f32_16x16x32_bf16 v[168:171], v[72:75], v[100:103], v[168:171]
	v_mfma_f32_16x16x32_bf16 v[172:175], v[76:79], v[100:103], v[172:175]
	s_add_u32 s42, s41, 0x14000
	buffer_load_dwordx4 v[28:31], v1, s[4:7], s42 offen sc0 nt
	v_mfma_f32_16x16x32_bf16 v[176:179], v[80:83], v[100:103], v[176:179]
	v_mfma_f32_16x16x32_bf16 v[180:183], v[84:87], v[100:103], v[180:183]
	v_mfma_f32_16x16x32_bf16 v[184:187], v[72:75], v[104:107], v[184:187]
	v_mfma_f32_16x16x32_bf16 v[188:191], v[76:79], v[104:107], v[188:191]
	buffer_load_dwordx4 v2, s[12:15], s44 offen offset:2048 sc1 lds
	v_mfma_f32_16x16x32_bf16 v[192:195], v[80:83], v[104:107], v[192:195]
	v_mfma_f32_16x16x32_bf16 v[196:199], v[84:87], v[104:107], v[196:199]
	v_mfma_f32_16x16x32_bf16 v[200:203], v[72:75], v[108:111], v[200:203]
	v_mfma_f32_16x16x32_bf16 v[204:207], v[76:79], v[108:111], v[204:207]
	s_add_u32 s42, s41, 0x18000
	buffer_load_dwordx4 v[32:35], v1, s[4:7], s42 offen sc0 nt
	v_mfma_f32_16x16x32_bf16 v[208:211], v[80:83], v[108:111], v[208:211]
	v_mfma_f32_16x16x32_bf16 v[212:215], v[84:87], v[108:111], v[212:215]
	v_mfma_f32_16x16x32_bf16 v[216:219], v[72:75], v[112:115], v[216:219]
	v_mfma_f32_16x16x32_bf16 v[220:223], v[76:79], v[112:115], v[220:223]
	buffer_load_dwordx4 v2, s[12:15], s44 offen offset:3072 sc1 lds
	v_mfma_f32_16x16x32_bf16 v[224:227], v[80:83], v[112:115], v[224:227]
	v_mfma_f32_16x16x32_bf16 v[228:231], v[84:87], v[112:115], v[228:231]
	v_mfma_f32_16x16x32_bf16 v[232:235], v[72:75], v[116:119], v[232:235]
	v_mfma_f32_16x16x32_bf16 v[236:239], v[76:79], v[116:119], v[236:239]
	s_add_u32 s42, s41, 0x1c000
	buffer_load_dwordx4 v[36:39], v1, s[4:7], s42 offen sc0 nt
	v_mfma_f32_16x16x32_bf16 v[240:243], v[80:83], v[116:119], v[240:243]
	s_add_u32 s26, s26, 0x8000
	s_cmp_eq_u32 s26, s32
	s_cselect_b32 s26, s27, s26
	v_mfma_f32_16x16x32_bf16 v[244:247], v[84:87], v[116:119], v[244:247]
	s_barrier
	s_sub_u32 s38, s38, 1
	s_cmp_lg_u32 s38, 0
	s_cbranch_scc1 .Lg_loop1
	v_add_u32_e32 v6, s33, v5
	ds_read_b128 v[72:75], v6 offset:0
	ds_read_b128 v[76:79], v6 offset:2048
	ds_read_b128 v[80:83], v6 offset:4096
	ds_read_b128 v[84:87], v6 offset:6144
	ds_read_b128 v[88:91], v4 offset:0
	ds_read_b128 v[92:95], v4 offset:2048
	ds_read_b128 v[96:99], v4 offset:4096
	ds_read_b128 v[100:103], v4 offset:6144
	ds_read_b128 v[104:107], v4 offset:8192
	ds_read_b128 v[108:111], v4 offset:10240
	ds_read_b128 v[112:115], v4 offset:12288
	ds_read_b128 v[116:119], v4 offset:14336
	s_waitcnt vmcnt(22)
	v_cvt_pk_bf16_f32 v40, v40, v41
	v_cvt_pk_bf16_f32 v41, v42, v43
	v_cvt_pk_bf16_f32 v44, v44, v45
	v_cvt_pk_bf16_f32 v45, v46, v47
	ds_write2st64_b64 v3, v[40:41], v[44:45] offset0:64 offset1:72
	s_waitcnt vmcnt(20)
	v_cvt_pk_bf16_f32 v48, v48, v49
	v_cvt_pk_bf16_f32 v49, v50, v51
	v_cvt_pk_bf16_f32 v52, v52, v53
	v_cvt_pk_bf16_f32 v53, v54, v55
	ds_write2st64_b64 v3, v[48:49], v[52:53] offset0:80 offset1:88
	s_waitcnt lgkmcnt(0)
	s_barrier
	v_mfma_f32_16x16x32_bf16 v[120:123], v[72:75], v[88:91], v[120:123]
	s_min_u32 s40, s25, 31
	s_bitcmp1_b32 s40, 4
	s_cselect_b32 s41, s23, s22
	s_lshl_b32 s42, s40, 23
	s_and_b32 s42, s42, 0x7000000
	s_or_b32 s41, s41, s42
	s_lshl_b32 s42, s40, 8
	s_and_b32 s42, s42, 0x100
	s_or_b32 s41, s41, s42
	s_sub_u32 s43, s25, 1
	s_min_u32 s43, s43, 31
	s_and_b32 s43, s43, 15
	s_lshl_b32 s43, s43, 15
	s_add_u32 s44, s43, s24
	v_mfma_f32_16x16x32_bf16 v[124:127], v[76:79], v[88:91], v[124:127]
	v_mfma_f32_16x16x32_bf16 v[128:131], v[80:83], v[88:91], v[128:131]
	v_mfma_f32_16x16x32_bf16 v[132:135], v[84:87], v[88:91], v[132:135]
	buffer_load_dwordx4 v[40:43], v1, s[4:7], s41 offen sc0 nt
	v_mfma_f32_16x16x32_bf16 v[136:139], v[72:75], v[92:95], v[136:139]
	v_mfma_f32_16x16x32_bf16 v[140:143], v[76:79], v[92:95], v[140:143]
	v_mfma_f32_16x16x32_bf16 v[144:147], v[80:83], v[92:95], v[144:147]
	v_mfma_f32_16x16x32_bf16 v[148:151], v[84:87], v[92:95], v[148:151]
	v_mfma_f32_16x16x32_bf16 v[152:155], v[72:75], v[96:99], v[152:155]
	v_mfma_f32_16x16x32_bf16 v[156:159], v[76:79], v[96:99], v[156:159]
	v_mfma_f32_16x16x32_bf16 v[160:163], v[80:83], v[96:99], v[160:163]
	v_mfma_f32_16x16x32_bf16 v[164:167], v[84:87], v[96:99], v[164:167]
	s_add_u32 s42, s41, 0x4000
	buffer_load_dwordx4 v[44:47], v1, s[4:7], s42 offen sc0 nt
	v_mfma_f32_16x16x32_bf16 v[168:171], v[72:75], v[100:103], v[168:171]
	v_mfma_f32_16x16x32_bf16 v[172:175], v[76:79], v[100:103], v[172:175]
	v_mfma_f32_16x16x32_bf16 v[176:179], v[80:83], v[100:103], v[176:179]
	v_mfma_f32_16x16x32_bf16 v[180:183], v[84:87], v[100:103], v[180:183]
	v_mfma_f32_16x16x32_bf16 v[184:187], v[72:75], v[104:107], v[184:187]
	v_mfma_f32_16x16x32_bf16 v[188:191], v[76:79], v[104:107], v[188:191]
	v_mfma_f32_16x16x32_bf16 v[192:195], v[80:83], v[104:107], v[192:195]
	v_mfma_f32_16x16x32_bf16 v[196:199], v[84:87], v[104:107], v[196:199]
	s_add_u32 s42, s41, 0x8000
	buffer_load_dwordx4 v[48:51], v1, s[4:7], s42 offen sc0 nt
	v_mfma_f32_16x16x32_bf16 v[200:203], v[72:75], v[108:111], v[200:203]
	v_mfma_f32_16x16x32_bf16 v[204:207], v[76:79], v[108:111], v[204:207]
	v_mfma_f32_16x16x32_bf16 v[208:211], v[80:83], v[108:111], v[208:211]
	v_mfma_f32_16x16x32_bf16 v[212:215], v[84:87], v[108:111], v[212:215]
	v_mfma_f32_16x16x32_bf16 v[216:219], v[72:75], v[112:115], v[216:219]
	v_mfma_f32_16x16x32_bf16 v[220:223], v[76:79], v[112:115], v[220:223]
	v_mfma_f32_16x16x32_bf16 v[224:227], v[80:83], v[112:115], v[224:227]
	v_mfma_f32_16x16x32_bf16 v[228:231], v[84:87], v[112:115], v[228:231]
	s_add_u32 s42, s41, 0xc000
	buffer_load_dwordx4 v[52:55], v1, s[4:7], s42 offen sc0 nt
	v_mfma_f32_16x16x32_bf16 v[232:235], v[72:75], v[116:119], v[232:235]
	v_mfma_f32_16x16x32_bf16 v[236:239], v[76:79], v[116:119], v[236:239]
	v_mfma_f32_16x16x32_bf16 v[240:243], v[80:83], v[116:119], v[240:243]
	v_mfma_f32_16x16x32_bf16 v[244:247], v[84:87], v[116:119], v[244:247]
	s_barrier
	ds_read_b128 v[72:75], v6 offset:1024
	ds_read_b128 v[76:79], v6 offset:3072
	ds_read_b128 v[80:83], v6 offset:5120
	ds_read_b128 v[84:87], v6 offset:7168
	ds_read_b128 v[88:91], v4 offset:1024
	ds_read_b128 v[92:95], v4 offset:3072
	ds_read_b128 v[96:99], v4 offset:5120
	ds_read_b128 v[100:103], v4 offset:7168
	ds_read_b128 v[104:107], v4 offset:9216
	ds_read_b128 v[108:111], v4 offset:11264
	ds_read_b128 v[112:115], v4 offset:13312
	ds_read_b128 v[116:119], v4 offset:15360
	s_waitcnt vmcnt(20)
	v_cvt_pk_bf16_f32 v56, v56, v57
	v_cvt_pk_bf16_f32 v57, v58, v59
	v_cvt_pk_bf16_f32 v60, v60, v61
	v_cvt_pk_bf16_f32 v61, v62, v63
	ds_write2st64_b64 v3, v[56:57], v[60:61] offset0:96 offset1:104
	s_waitcnt vmcnt(16)
	v_cvt_pk_bf16_f32 v64, v64, v65
	v_cvt_pk_bf16_f32 v65, v66, v67
	v_cvt_pk_bf16_f32 v68, v68, v69
	v_cvt_pk_bf16_f32 v69, v70, v71
	ds_write2st64_b64 v3, v[64:65], v[68:69] offset0:112 offset1:120
	s_waitcnt vmcnt(5)
	s_waitcnt lgkmcnt(0)
	s_barrier
	v_mfma_f32_16x16x32_bf16 v[120:123], v[72:75], v[88:91], v[120:123]
	s_add_u32 s33, s33, 0x8000
	s_cmp_eq_u32 s33, 0x18000
	s_cselect_b32 s33, 0, s33
	s_add_u32 s25, s25, 1
	s_mov_b32 m0, s26
	v_mfma_f32_16x16x32_bf16 v[124:127], v[76:79], v[88:91], v[124:127]
	buffer_load_dwordx4 v2, s[12:15], s44 offen sc1 lds
	v_mfma_f32_16x16x32_bf16 v[128:131], v[80:83], v[88:91], v[128:131]
	v_mfma_f32_16x16x32_bf16 v[132:135], v[84:87], v[88:91], v[132:135]
	v_mfma_f32_16x16x32_bf16 v[136:139], v[72:75], v[92:95], v[136:139]
	v_mfma_f32_16x16x32_bf16 v[140:143], v[76:79], v[92:95], v[140:143]
	s_add_u32 s42, s41, 0x10000
	buffer_load_dwordx4 v[56:59], v1, s[4:7], s42 offen sc0 nt
	v_mfma_f32_16x16x32_bf16 v[144:147], v[80:83], v[92:95], v[144:147]
	v_mfma_f32_16x16x32_bf16 v[148:151], v[84:87], v[92:95], v[148:151]
	v_mfma_f32_16x16x32_bf16 v[152:155], v[72:75], v[96:99], v[152:155]
	v_mfma_f32_16x16x32_bf16 v[156:159], v[76:79], v[96:99], v[156:159]
	buffer_load_dwordx4 v2, s[12:15], s44 offen offset:1024 sc1 lds
	v_mfma_f32_16x16x32_bf16 v[160:163], v[80:83], v[96:99], v[160:163]
	v_mfma_f32_16x16x32_bf16 v[164:167], v[84:87], v[96:99], v[164:167]
	v_mfma_f32_16x16x32_bf16 v[168:171], v[72:75], v[100:103], v[168:171]
	v_mfma_f32_16x16x32_bf16 v[172:175], v[76:79], v[100:103], v[172:175]
	s_add_u32 s42, s41, 0x14000
	buffer_load_dwordx4 v[60:63], v1, s[4:7], s42 offen sc0 nt
	v_mfma_f32_16x16x32_bf16 v[176:179], v[80:83], v[100:103], v[176:179]
	v_mfma_f32_16x16x32_bf16 v[180:183], v[84:87], v[100:103], v[180:183]
	v_mfma_f32_16x16x32_bf16 v[184:187], v[72:75], v[104:107], v[184:187]
	v_mfma_f32_16x16x32_bf16 v[188:191], v[76:79], v[104:107], v[188:191]
	buffer_load_dwordx4 v2, s[12:15], s44 offen offset:2048 sc1 lds
	v_mfma_f32_16x16x32_bf16 v[192:195], v[80:83], v[104:107], v[192:195]
	v_mfma_f32_16x16x32_bf16 v[196:199], v[84:87], v[104:107], v[196:199]
	v_mfma_f32_16x16x32_bf16 v[200:203], v[72:75], v[108:111], v[200:203]
	v_mfma_f32_16x16x32_bf16 v[204:207], v[76:79], v[108:111], v[204:207]
	s_add_u32 s42, s41, 0x18000
	buffer_load_dwordx4 v[64:67], v1, s[4:7], s42 offen sc0 nt
	v_mfma_f32_16x16x32_bf16 v[208:211], v[80:83], v[108:111], v[208:211]
	v_mfma_f32_16x16x32_bf16 v[212:215], v[84:87], v[108:111], v[212:215]
	v_mfma_f32_16x16x32_bf16 v[216:219], v[72:75], v[112:115], v[216:219]
	v_mfma_f32_16x16x32_bf16 v[220:223], v[76:79], v[112:115], v[220:223]
	buffer_load_dwordx4 v2, s[12:15], s44 offen offset:3072 sc1 lds
	v_mfma_f32_16x16x32_bf16 v[224:227], v[80:83], v[112:115], v[224:227]
	v_mfma_f32_16x16x32_bf16 v[228:231], v[84:87], v[112:115], v[228:231]
	v_mfma_f32_16x16x32_bf16 v[232:235], v[72:75], v[116:119], v[232:235]
	v_mfma_f32_16x16x32_bf16 v[236:239], v[76:79], v[116:119], v[236:239]
	s_add_u32 s42, s41, 0x1c000
	buffer_load_dwordx4 v[68:71], v1, s[4:7], s42 offen sc0 nt
	v_mfma_f32_16x16x32_bf16 v[240:243], v[80:83], v[116:119], v[240:243]
	s_add_u32 s26, s26, 0x8000
	s_cmp_eq_u32 s26, s32
	s_cselect_b32 s26, s27, s26
	v_mfma_f32_16x16x32_bf16 v[244:247], v[84:87], v[116:119], v[244:247]
	s_barrier
	v_add_u32_e32 v6, s33, v5
	ds_read_b128 v[72:75], v6 offset:0
	ds_read_b128 v[76:79], v6 offset:2048
	ds_read_b128 v[80:83], v6 offset:4096
	ds_read_b128 v[84:87], v6 offset:6144
	ds_read_b128 v[88:91], v4 offset:32768
	ds_read_b128 v[92:95], v4 offset:34816
	ds_read_b128 v[96:99], v4 offset:36864
	ds_read_b128 v[100:103], v4 offset:38912
	ds_read_b128 v[104:107], v4 offset:40960
	ds_read_b128 v[108:111], v4 offset:43008
	ds_read_b128 v[112:115], v4 offset:45056
	ds_read_b128 v[116:119], v4 offset:47104
	s_waitcnt vmcnt(22)
	v_cvt_pk_bf16_f32 v8, v8, v9
	v_cvt_pk_bf16_f32 v9, v10, v11
	v_cvt_pk_bf16_f32 v12, v12, v13
	v_cvt_pk_bf16_f32 v13, v14, v15
	ds_write2st64_b64 v3, v[8:9], v[12:13] offset0:0 offset1:8
	s_waitcnt vmcnt(20)
	v_cvt_pk_bf16_f32 v16, v16, v17
	v_cvt_pk_bf16_f32 v17, v18, v19
	v_cvt_pk_bf16_f32 v20, v20, v21
	v_cvt_pk_bf16_f32 v21, v22, v23
	ds_write2st64_b64 v3, v[16:17], v[20:21] offset0:16 offset1:24
	s_waitcnt lgkmcnt(0)
	s_barrier
	v_mfma_f32_16x16x32_bf16 v[120:123], v[72:75], v[88:91], v[120:123]
	s_min_u32 s40, s25, 31
	s_bitcmp1_b32 s40, 4
	s_cselect_b32 s41, s23, s22
	s_lshl_b32 s42, s40, 23
	s_and_b32 s42, s42, 0x7000000
	s_or_b32 s41, s41, s42
	s_lshl_b32 s42, s40, 8
	s_and_b32 s42, s42, 0x100
	s_or_b32 s41, s41, s42
	s_sub_u32 s43, s25, 1
	s_min_u32 s43, s43, 31
	s_and_b32 s43, s43, 15
	s_lshl_b32 s43, s43, 15
	s_add_u32 s44, s43, s24
	v_mfma_f32_16x16x32_bf16 v[124:127], v[76:79], v[88:91], v[124:127]
	v_mfma_f32_16x16x32_bf16 v[128:131], v[80:83], v[88:91], v[128:131]
	v_mfma_f32_16x16x32_bf16 v[132:135], v[84:87], v[88:91], v[132:135]
	v_mfma_f32_16x16x32_bf16 v[136:139], v[72:75], v[92:95], v[136:139]
	v_mfma_f32_16x16x32_bf16 v[140:143], v[76:79], v[92:95], v[140:143]
	v_mfma_f32_16x16x32_bf16 v[144:147], v[80:83], v[92:95], v[144:147]
	v_mfma_f32_16x16x32_bf16 v[148:151], v[84:87], v[92:95], v[148:151]
	v_mfma_f32_16x16x32_bf16 v[152:155], v[72:75], v[96:99], v[152:155]
	v_mfma_f32_16x16x32_bf16 v[156:159], v[76:79], v[96:99], v[156:159]
	v_mfma_f32_16x16x32_bf16 v[160:163], v[80:83], v[96:99], v[160:163]
	v_mfma_f32_16x16x32_bf16 v[164:167], v[84:87], v[96:99], v[164:167]
	v_mfma_f32_16x16x32_bf16 v[168:171], v[72:75], v[100:103], v[168:171]
	v_mfma_f32_16x16x32_bf16 v[172:175], v[76:79], v[100:103], v[172:175]
	v_mfma_f32_16x16x32_bf16 v[176:179], v[80:83], v[100:103], v[176:179]
	v_mfma_f32_16x16x32_bf16 v[180:183], v[84:87], v[100:103], v[180:183]
	v_mfma_f32_16x16x32_bf16 v[184:187], v[72:75], v[104:107], v[184:187]
	v_mfma_f32_16x16x32_bf16 v[188:191], v[76:79], v[104:107], v[188:191]
	v_mfma_f32_16x16x32_bf16 v[192:195], v[80:83], v[104:107], v[192:195]
	v_mfma_f32_16x16x32_bf16 v[196:199], v[84:87], v[104:107], v[196:199]
	v_mfma_f32_16x16x32_bf16 v[200:203], v[72:75], v[108:111], v[200:203]
	v_mfma_f32_16x16x32_bf16 v[204:207], v[76:79], v[108:111], v[204:207]
	v_mfma_f32_16x16x32_bf16 v[208:211], v[80:83], v[108:111], v[208:211]
	v_mfma_f32_16x16x32_bf16 v[212:215], v[84:87], v[108:111], v[212:215]
	v_mfma_f32_16x16x32_bf16 v[216:219], v[72:75], v[112:115], v[216:219]
	v_mfma_f32_16x16x32_bf16 v[220:223], v[76:79], v[112:115], v[220:223]
	v_mfma_f32_16x16x32_bf16 v[224:227], v[80:83], v[112:115], v[224:227]
	v_mfma_f32_16x16x32_bf16 v[228:231], v[84:87], v[112:115], v[228:231]
	v_mfma_f32_16x16x32_bf16 v[232:235], v[72:75], v[116:119], v[232:235]
	v_mfma_f32_16x16x32_bf16 v[236:239], v[76:79], v[116:119], v[236:239]
	v_mfma_f32_16x16x32_bf16 v[240:243], v[80:83], v[116:119], v[240:243]
	v_mfma_f32_16x16x32_bf16 v[244:247], v[84:87], v[116:119], v[244:247]
	s_barrier
	ds_read_b128 v[72:75], v6 offset:1024
	ds_read_b128 v[76:79], v6 offset:3072
	ds_read_b128 v[80:83], v6 offset:5120
	ds_read_b128 v[84:87], v6 offset:7168
	ds_read_b128 v[88:91], v4 offset:33792
	ds_read_b128 v[92:95], v4 offset:35840
	ds_read_b128 v[96:99], v4 offset:37888
	ds_read_b128 v[100:103], v4 offset:39936
	ds_read_b128 v[104:107], v4 offset:41984
	ds_read_b128 v[108:111], v4 offset:44032
	ds_read_b128 v[112:115], v4 offset:46080
	ds_read_b128 v[116:119], v4 offset:48128
	s_waitcnt vmcnt(16)
	v_cvt_pk_bf16_f32 v24, v24, v25
	v_cvt_pk_bf16_f32 v25, v26, v27
	v_cvt_pk_bf16_f32 v28, v28, v29
	v_cvt_pk_bf16_f32 v29, v30, v31
	ds_write2st64_b64 v3, v[24:25], v[28:29] offset0:32 offset1:40
	s_waitcnt vmcnt(12)
	v_cvt_pk_bf16_f32 v32, v32, v33
	v_cvt_pk_bf16_f32 v33, v34, v35
	v_cvt_pk_bf16_f32 v36, v36, v37
	v_cvt_pk_bf16_f32 v37, v38, v39
	ds_write2st64_b64 v3, v[32:33], v[36:37] offset0:48 offset1:56
	s_waitcnt vmcnt(1)
	s_waitcnt lgkmcnt(0)
	s_barrier
	v_mfma_f32_16x16x32_bf16 v[120:123], v[72:75], v[88:91], v[120:123]
	s_add_u32 s33, s33, 0x8000
	s_cmp_eq_u32 s33, 0x18000
	s_cselect_b32 s33, 0, s33
	s_add_u32 s25, s25, 1
	s_mov_b32 m0, s26
	v_mfma_f32_16x16x32_bf16 v[124:127], v[76:79], v[88:91], v[124:127]
	buffer_load_dwordx4 v2, s[12:15], s44 offen sc1 lds
	v_mfma_f32_16x16x32_bf16 v[128:131], v[80:83], v[88:91], v[128:131]
	v_mfma_f32_16x16x32_bf16 v[132:135], v[84:87], v[88:91], v[132:135]
	v_mfma_f32_16x16x32_bf16 v[136:139], v[72:75], v[92:95], v[136:139]
	v_mfma_f32_16x16x32_bf16 v[140:143], v[76:79], v[92:95], v[140:143]
	v_mfma_f32_16x16x32_bf16 v[144:147], v[80:83], v[92:95], v[144:147]
	v_mfma_f32_16x16x32_bf16 v[148:151], v[84:87], v[92:95], v[148:151]
	v_mfma_f32_16x16x32_bf16 v[152:155], v[72:75], v[96:99], v[152:155]
	v_mfma_f32_16x16x32_bf16 v[156:159], v[76:79], v[96:99], v[156:159]
	buffer_load_dwordx4 v2, s[12:15], s44 offen offset:1024 sc1 lds
	v_mfma_f32_16x16x32_bf16 v[160:163], v[80:83], v[96:99], v[160:163]
	v_mfma_f32_16x16x32_bf16 v[164:167], v[84:87], v[96:99], v[164:167]
	v_mfma_f32_16x16x32_bf16 v[168:171], v[72:75], v[100:103], v[168:171]
	v_mfma_f32_16x16x32_bf16 v[172:175], v[76:79], v[100:103], v[172:175]
	v_mfma_f32_16x16x32_bf16 v[176:179], v[80:83], v[100:103], v[176:179]
	v_mfma_f32_16x16x32_bf16 v[180:183], v[84:87], v[100:103], v[180:183]
	v_mfma_f32_16x16x32_bf16 v[184:187], v[72:75], v[104:107], v[184:187]
	v_mfma_f32_16x16x32_bf16 v[188:191], v[76:79], v[104:107], v[188:191]
	buffer_load_dwordx4 v2, s[12:15], s44 offen offset:2048 sc1 lds
	v_mfma_f32_16x16x32_bf16 v[192:195], v[80:83], v[104:107], v[192:195]
	v_mfma_f32_16x16x32_bf16 v[196:199], v[84:87], v[104:107], v[196:199]
	v_mfma_f32_16x16x32_bf16 v[200:203], v[72:75], v[108:111], v[200:203]
	v_mfma_f32_16x16x32_bf16 v[204:207], v[76:79], v[108:111], v[204:207]
	v_mfma_f32_16x16x32_bf16 v[208:211], v[80:83], v[108:111], v[208:211]
	v_mfma_f32_16x16x32_bf16 v[212:215], v[84:87], v[108:111], v[212:215]
	v_mfma_f32_16x16x32_bf16 v[216:219], v[72:75], v[112:115], v[216:219]
	v_mfma_f32_16x16x32_bf16 v[220:223], v[76:79], v[112:115], v[220:223]
	buffer_load_dwordx4 v2, s[12:15], s44 offen offset:3072 sc1 lds
	v_mfma_f32_16x16x32_bf16 v[224:227], v[80:83], v[112:115], v[224:227]
	v_mfma_f32_16x16x32_bf16 v[228:231], v[84:87], v[112:115], v[228:231]
	v_mfma_f32_16x16x32_bf16 v[232:235], v[72:75], v[116:119], v[232:235]
	v_mfma_f32_16x16x32_bf16 v[236:239], v[76:79], v[116:119], v[236:239]
	v_mfma_f32_16x16x32_bf16 v[240:243], v[80:83], v[116:119], v[240:243]
	s_add_u32 s26, s26, 0x8000
	s_cmp_eq_u32 s26, s32
	s_cselect_b32 s26, s27, s26
	v_mfma_f32_16x16x32_bf16 v[244:247], v[84:87], v[116:119], v[244:247]
	s_barrier
	v_add_u32_e32 v6, s33, v5
	ds_read_b128 v[72:75], v6 offset:0
	ds_read_b128 v[76:79], v6 offset:2048
	ds_read_b128 v[80:83], v6 offset:4096
	ds_read_b128 v[84:87], v6 offset:6144
	ds_read_b128 v[88:91], v4 offset:0
	ds_read_b128 v[92:95], v4 offset:2048
	ds_read_b128 v[96:99], v4 offset:4096
	ds_read_b128 v[100:103], v4 offset:6144
	ds_read_b128 v[104:107], v4 offset:8192
	ds_read_b128 v[108:111], v4 offset:10240
	ds_read_b128 v[112:115], v4 offset:12288
	ds_read_b128 v[116:119], v4 offset:14336
	s_waitcnt vmcnt(14)
	v_cvt_pk_bf16_f32 v40, v40, v41
	v_cvt_pk_bf16_f32 v41, v42, v43
	v_cvt_pk_bf16_f32 v44, v44, v45
	v_cvt_pk_bf16_f32 v45, v46, v47
	ds_write2st64_b64 v3, v[40:41], v[44:45] offset0:64 offset1:72
	s_waitcnt vmcnt(12)
	v_cvt_pk_bf16_f32 v48, v48, v49
	v_cvt_pk_bf16_f32 v49, v50, v51
	v_cvt_pk_bf16_f32 v52, v52, v53
	v_cvt_pk_bf16_f32 v53, v54, v55
	ds_write2st64_b64 v3, v[48:49], v[52:53] offset0:80 offset1:88
	s_waitcnt lgkmcnt(0)
	s_barrier
	v_mfma_f32_16x16x32_bf16 v[120:123], v[72:75], v[88:91], v[120:123]
	v_mfma_f32_16x16x32_bf16 v[124:127], v[76:79], v[88:91], v[124:127]
	v_mfma_f32_16x16x32_bf16 v[128:131], v[80:83], v[88:91], v[128:131]
	v_mfma_f32_16x16x32_bf16 v[132:135], v[84:87], v[88:91], v[132:135]
	v_mfma_f32_16x16x32_bf16 v[136:139], v[72:75], v[92:95], v[136:139]
	v_mfma_f32_16x16x32_bf16 v[140:143], v[76:79], v[92:95], v[140:143]
	v_mfma_f32_16x16x32_bf16 v[144:147], v[80:83], v[92:95], v[144:147]
	v_mfma_f32_16x16x32_bf16 v[148:151], v[84:87], v[92:95], v[148:151]
	v_mfma_f32_16x16x32_bf16 v[152:155], v[72:75], v[96:99], v[152:155]
	v_mfma_f32_16x16x32_bf16 v[156:159], v[76:79], v[96:99], v[156:159]
	v_mfma_f32_16x16x32_bf16 v[160:163], v[80:83], v[96:99], v[160:163]
	v_mfma_f32_16x16x32_bf16 v[164:167], v[84:87], v[96:99], v[164:167]
	v_mfma_f32_16x16x32_bf16 v[168:171], v[72:75], v[100:103], v[168:171]
	v_mfma_f32_16x16x32_bf16 v[172:175], v[76:79], v[100:103], v[172:175]
	v_mfma_f32_16x16x32_bf16 v[176:179], v[80:83], v[100:103], v[176:179]
	v_mfma_f32_16x16x32_bf16 v[180:183], v[84:87], v[100:103], v[180:183]
	v_mfma_f32_16x16x32_bf16 v[184:187], v[72:75], v[104:107], v[184:187]
	v_mfma_f32_16x16x32_bf16 v[188:191], v[76:79], v[104:107], v[188:191]
	v_mfma_f32_16x16x32_bf16 v[192:195], v[80:83], v[104:107], v[192:195]
	v_mfma_f32_16x16x32_bf16 v[196:199], v[84:87], v[104:107], v[196:199]
	v_mfma_f32_16x16x32_bf16 v[200:203], v[72:75], v[108:111], v[200:203]
	v_mfma_f32_16x16x32_bf16 v[204:207], v[76:79], v[108:111], v[204:207]
	v_mfma_f32_16x16x32_bf16 v[208:211], v[80:83], v[108:111], v[208:211]
	v_mfma_f32_16x16x32_bf16 v[212:215], v[84:87], v[108:111], v[212:215]
	v_mfma_f32_16x16x32_bf16 v[216:219], v[72:75], v[112:115], v[216:219]
	v_mfma_f32_16x16x32_bf16 v[220:223], v[76:79], v[112:115], v[220:223]
	v_mfma_f32_16x16x32_bf16 v[224:227], v[80:83], v[112:115], v[224:227]
	v_mfma_f32_16x16x32_bf16 v[228:231], v[84:87], v[112:115], v[228:231]
	v_mfma_f32_16x16x32_bf16 v[232:235], v[72:75], v[116:119], v[232:235]
	v_mfma_f32_16x16x32_bf16 v[236:239], v[76:79], v[116:119], v[236:239]
	v_mfma_f32_16x16x32_bf16 v[240:243], v[80:83], v[116:119], v[240:243]
	v_mfma_f32_16x16x32_bf16 v[244:247], v[84:87], v[116:119], v[244:247]
	s_barrier
	ds_read_b128 v[72:75], v6 offset:1024
	ds_read_b128 v[76:79], v6 offset:3072
	ds_read_b128 v[80:83], v6 offset:5120
	ds_read_b128 v[84:87], v6 offset:7168
	ds_read_b128 v[88:91], v4 offset:1024
	ds_read_b128 v[92:95], v4 offset:3072
	ds_read_b128 v[96:99], v4 offset:5120
	ds_read_b128 v[100:103], v4 offset:7168
	ds_read_b128 v[104:107], v4 offset:9216
	ds_read_b128 v[108:111], v4 offset:11264
	ds_read_b128 v[112:115], v4 offset:13312
	ds_read_b128 v[116:119], v4 offset:15360
	s_waitcnt vmcnt(8)
	v_cvt_pk_bf16_f32 v56, v56, v57
	v_cvt_pk_bf16_f32 v57, v58, v59
	v_cvt_pk_bf16_f32 v60, v60, v61
	v_cvt_pk_bf16_f32 v61, v62, v63
	ds_write2st64_b64 v3, v[56:57], v[60:61] offset0:96 offset1:104
	s_waitcnt vmcnt(4)
	v_cvt_pk_bf16_f32 v64, v64, v65
	v_cvt_pk_bf16_f32 v65, v66, v67
	v_cvt_pk_bf16_f32 v68, v68, v69
	v_cvt_pk_bf16_f32 v69, v70, v71
	ds_write2st64_b64 v3, v[64:65], v[68:69] offset0:112 offset1:120
	s_waitcnt vmcnt(0)
	s_waitcnt lgkmcnt(0)
	s_barrier
	v_mfma_f32_16x16x32_bf16 v[120:123], v[72:75], v[88:91], v[120:123]
	s_add_u32 s33, s33, 0x8000
	s_cmp_eq_u32 s33, 0x18000
	s_cselect_b32 s33, 0, s33
	s_add_u32 s25, s25, 1
	v_mfma_f32_16x16x32_bf16 v[124:127], v[76:79], v[88:91], v[124:127]
	v_mfma_f32_16x16x32_bf16 v[128:131], v[80:83], v[88:91], v[128:131]
	v_mfma_f32_16x16x32_bf16 v[132:135], v[84:87], v[88:91], v[132:135]
	v_mfma_f32_16x16x32_bf16 v[136:139], v[72:75], v[92:95], v[136:139]
	v_mfma_f32_16x16x32_bf16 v[140:143], v[76:79], v[92:95], v[140:143]
	v_mfma_f32_16x16x32_bf16 v[144:147], v[80:83], v[92:95], v[144:147]
	v_mfma_f32_16x16x32_bf16 v[148:151], v[84:87], v[92:95], v[148:151]
	v_mfma_f32_16x16x32_bf16 v[152:155], v[72:75], v[96:99], v[152:155]
	v_mfma_f32_16x16x32_bf16 v[156:159], v[76:79], v[96:99], v[156:159]
	v_mfma_f32_16x16x32_bf16 v[160:163], v[80:83], v[96:99], v[160:163]
	v_mfma_f32_16x16x32_bf16 v[164:167], v[84:87], v[96:99], v[164:167]
	v_mfma_f32_16x16x32_bf16 v[168:171], v[72:75], v[100:103], v[168:171]
	v_mfma_f32_16x16x32_bf16 v[172:175], v[76:79], v[100:103], v[172:175]
	v_mfma_f32_16x16x32_bf16 v[176:179], v[80:83], v[100:103], v[176:179]
	v_mfma_f32_16x16x32_bf16 v[180:183], v[84:87], v[100:103], v[180:183]
	v_mfma_f32_16x16x32_bf16 v[184:187], v[72:75], v[104:107], v[184:187]
	v_mfma_f32_16x16x32_bf16 v[188:191], v[76:79], v[104:107], v[188:191]
	v_mfma_f32_16x16x32_bf16 v[192:195], v[80:83], v[104:107], v[192:195]
	v_mfma_f32_16x16x32_bf16 v[196:199], v[84:87], v[104:107], v[196:199]
	v_mfma_f32_16x16x32_bf16 v[200:203], v[72:75], v[108:111], v[200:203]
	v_mfma_f32_16x16x32_bf16 v[204:207], v[76:79], v[108:111], v[204:207]
	v_mfma_f32_16x16x32_bf16 v[208:211], v[80:83], v[108:111], v[208:211]
	v_mfma_f32_16x16x32_bf16 v[212:215], v[84:87], v[108:111], v[212:215]
	v_mfma_f32_16x16x32_bf16 v[216:219], v[72:75], v[112:115], v[216:219]
	v_mfma_f32_16x16x32_bf16 v[220:223], v[76:79], v[112:115], v[220:223]
	v_mfma_f32_16x16x32_bf16 v[224:227], v[80:83], v[112:115], v[224:227]
	v_mfma_f32_16x16x32_bf16 v[228:231], v[84:87], v[112:115], v[228:231]
	v_mfma_f32_16x16x32_bf16 v[232:235], v[72:75], v[116:119], v[232:235]
	v_mfma_f32_16x16x32_bf16 v[236:239], v[76:79], v[116:119], v[236:239]
	v_mfma_f32_16x16x32_bf16 v[240:243], v[80:83], v[116:119], v[240:243]
	s_add_u32 s26, s26, 0x8000
	s_cmp_eq_u32 s26, s32
	s_cselect_b32 s26, s27, s26
	v_mfma_f32_16x16x32_bf16 v[244:247], v[84:87], v[116:119], v[244:247]
	s_barrier
	v_add_u32_e32 v6, s33, v5
	ds_read_b128 v[72:75], v6 offset:0
	ds_read_b128 v[76:79], v6 offset:2048
	ds_read_b128 v[80:83], v6 offset:4096
	ds_read_b128 v[84:87], v6 offset:6144
	ds_read_b128 v[88:91], v4 offset:32768
	ds_read_b128 v[92:95], v4 offset:34816
	ds_read_b128 v[96:99], v4 offset:36864
	ds_read_b128 v[100:103], v4 offset:38912
	ds_read_b128 v[104:107], v4 offset:40960
	ds_read_b128 v[108:111], v4 offset:43008
	ds_read_b128 v[112:115], v4 offset:45056
	ds_read_b128 v[116:119], v4 offset:47104
	s_waitcnt lgkmcnt(0)
	s_barrier
	v_mfma_f32_16x16x32_bf16 v[120:123], v[72:75], v[88:91], v[120:123]
	v_mfma_f32_16x16x32_bf16 v[124:127], v[76:79], v[88:91], v[124:127]
	v_mfma_f32_16x16x32_bf16 v[128:131], v[80:83], v[88:91], v[128:131]
	v_mfma_f32_16x16x32_bf16 v[132:135], v[84:87], v[88:91], v[132:135]
	v_mfma_f32_16x16x32_bf16 v[136:139], v[72:75], v[92:95], v[136:139]
	v_mfma_f32_16x16x32_bf16 v[140:143], v[76:79], v[92:95], v[140:143]
	v_mfma_f32_16x16x32_bf16 v[144:147], v[80:83], v[92:95], v[144:147]
	v_mfma_f32_16x16x32_bf16 v[148:151], v[84:87], v[92:95], v[148:151]
	v_mfma_f32_16x16x32_bf16 v[152:155], v[72:75], v[96:99], v[152:155]
	v_mfma_f32_16x16x32_bf16 v[156:159], v[76:79], v[96:99], v[156:159]
	v_mfma_f32_16x16x32_bf16 v[160:163], v[80:83], v[96:99], v[160:163]
	v_mfma_f32_16x16x32_bf16 v[164:167], v[84:87], v[96:99], v[164:167]
	v_mfma_f32_16x16x32_bf16 v[168:171], v[72:75], v[100:103], v[168:171]
	v_mfma_f32_16x16x32_bf16 v[172:175], v[76:79], v[100:103], v[172:175]
	v_mfma_f32_16x16x32_bf16 v[176:179], v[80:83], v[100:103], v[176:179]
	v_mfma_f32_16x16x32_bf16 v[180:183], v[84:87], v[100:103], v[180:183]
	v_mfma_f32_16x16x32_bf16 v[184:187], v[72:75], v[104:107], v[184:187]
	v_mfma_f32_16x16x32_bf16 v[188:191], v[76:79], v[104:107], v[188:191]
	v_mfma_f32_16x16x32_bf16 v[192:195], v[80:83], v[104:107], v[192:195]
	v_mfma_f32_16x16x32_bf16 v[196:199], v[84:87], v[104:107], v[196:199]
	v_mfma_f32_16x16x32_bf16 v[200:203], v[72:75], v[108:111], v[200:203]
	v_mfma_f32_16x16x32_bf16 v[204:207], v[76:79], v[108:111], v[204:207]
	v_mfma_f32_16x16x32_bf16 v[208:211], v[80:83], v[108:111], v[208:211]
	v_mfma_f32_16x16x32_bf16 v[212:215], v[84:87], v[108:111], v[212:215]
	v_mfma_f32_16x16x32_bf16 v[216:219], v[72:75], v[112:115], v[216:219]
	v_mfma_f32_16x16x32_bf16 v[220:223], v[76:79], v[112:115], v[220:223]
	v_mfma_f32_16x16x32_bf16 v[224:227], v[80:83], v[112:115], v[224:227]
	v_mfma_f32_16x16x32_bf16 v[228:231], v[84:87], v[112:115], v[228:231]
	v_mfma_f32_16x16x32_bf16 v[232:235], v[72:75], v[116:119], v[232:235]
	v_mfma_f32_16x16x32_bf16 v[236:239], v[76:79], v[116:119], v[236:239]
	v_mfma_f32_16x16x32_bf16 v[240:243], v[80:83], v[116:119], v[240:243]
	v_mfma_f32_16x16x32_bf16 v[244:247], v[84:87], v[116:119], v[244:247]
	s_barrier
	ds_read_b128 v[72:75], v6 offset:1024
	ds_read_b128 v[76:79], v6 offset:3072
	ds_read_b128 v[80:83], v6 offset:5120
	ds_read_b128 v[84:87], v6 offset:7168
	ds_read_b128 v[88:91], v4 offset:33792
	ds_read_b128 v[92:95], v4 offset:35840
	ds_read_b128 v[96:99], v4 offset:37888
	ds_read_b128 v[100:103], v4 offset:39936
	ds_read_b128 v[104:107], v4 offset:41984
	ds_read_b128 v[108:111], v4 offset:44032
	ds_read_b128 v[112:115], v4 offset:46080
	ds_read_b128 v[116:119], v4 offset:48128
	s_waitcnt lgkmcnt(0)
	s_barrier
	v_mfma_f32_16x16x32_bf16 v[120:123], v[72:75], v[88:91], v[120:123]
	s_add_u32 s33, s33, 0x8000
	s_cmp_eq_u32 s33, 0x18000
	s_cselect_b32 s33, 0, s33
	s_add_u32 s25, s25, 1
	v_mfma_f32_16x16x32_bf16 v[124:127], v[76:79], v[88:91], v[124:127]
	v_mfma_f32_16x16x32_bf16 v[128:131], v[80:83], v[88:91], v[128:131]
	v_mfma_f32_16x16x32_bf16 v[132:135], v[84:87], v[88:91], v[132:135]
	v_mfma_f32_16x16x32_bf16 v[136:139], v[72:75], v[92:95], v[136:139]
	v_mfma_f32_16x16x32_bf16 v[140:143], v[76:79], v[92:95], v[140:143]
	v_mfma_f32_16x16x32_bf16 v[144:147], v[80:83], v[92:95], v[144:147]
	v_mfma_f32_16x16x32_bf16 v[148:151], v[84:87], v[92:95], v[148:151]
	v_mfma_f32_16x16x32_bf16 v[152:155], v[72:75], v[96:99], v[152:155]
	v_mfma_f32_16x16x32_bf16 v[156:159], v[76:79], v[96:99], v[156:159]
	v_mfma_f32_16x16x32_bf16 v[160:163], v[80:83], v[96:99], v[160:163]
	v_mfma_f32_16x16x32_bf16 v[164:167], v[84:87], v[96:99], v[164:167]
	v_mfma_f32_16x16x32_bf16 v[168:171], v[72:75], v[100:103], v[168:171]
	v_mfma_f32_16x16x32_bf16 v[172:175], v[76:79], v[100:103], v[172:175]
	v_mfma_f32_16x16x32_bf16 v[176:179], v[80:83], v[100:103], v[176:179]
	v_mfma_f32_16x16x32_bf16 v[180:183], v[84:87], v[100:103], v[180:183]
	v_mfma_f32_16x16x32_bf16 v[184:187], v[72:75], v[104:107], v[184:187]
	v_mfma_f32_16x16x32_bf16 v[188:191], v[76:79], v[104:107], v[188:191]
	v_mfma_f32_16x16x32_bf16 v[192:195], v[80:83], v[104:107], v[192:195]
	v_mfma_f32_16x16x32_bf16 v[196:199], v[84:87], v[104:107], v[196:199]
	v_mfma_f32_16x16x32_bf16 v[200:203], v[72:75], v[108:111], v[200:203]
	v_mfma_f32_16x16x32_bf16 v[204:207], v[76:79], v[108:111], v[204:207]
	v_mfma_f32_16x16x32_bf16 v[208:211], v[80:83], v[108:111], v[208:211]
	v_mfma_f32_16x16x32_bf16 v[212:215], v[84:87], v[108:111], v[212:215]
	v_mfma_f32_16x16x32_bf16 v[216:219], v[72:75], v[112:115], v[216:219]
	v_mfma_f32_16x16x32_bf16 v[220:223], v[76:79], v[112:115], v[220:223]
	v_mfma_f32_16x16x32_bf16 v[224:227], v[80:83], v[112:115], v[224:227]
	v_mfma_f32_16x16x32_bf16 v[228:231], v[84:87], v[112:115], v[228:231]
	v_mfma_f32_16x16x32_bf16 v[232:235], v[72:75], v[116:119], v[232:235]
	v_mfma_f32_16x16x32_bf16 v[236:239], v[76:79], v[116:119], v[236:239]
	v_mfma_f32_16x16x32_bf16 v[240:243], v[80:83], v[116:119], v[240:243]
	s_add_u32 s26, s26, 0x8000
	s_cmp_eq_u32 s26, s32
	s_cselect_b32 s26, s27, s26
	v_mfma_f32_16x16x32_bf16 v[244:247], v[84:87], v[116:119], v[244:247]
	s_barrier
	s_cmp_ge_u32 s21, 4
	s_cbranch_scc1 .Lg_fin2
	s_barrier
